# attention units: per-block s_setprio 1/0 flips removed (on top of the VALU/MFMA interleave)
# speedup vs baseline: 1.0057x; 1.0018x over previous
; #define LAS __attribute__((address_space(3)))
; #define TIDX(wv) (((wv) << 6) | lane_id())
; __device__ __forceinline__ int v_st(int k, int c) { const int kk = (k & ~0xC) | ((k & 4) << 1) | ((k & 8) >> 1); return ((kk >> 3) * 2 + (c >> 5)) * 512 + ((kk & 7) * 32 + (c & 31)) * 2; }
; __device__ __forceinline__ int v_rd_base(int lane) { return ((lane & 3) << 3) | (((lane >> 2) & 3) << 6) | (((lane >> 4) & 1) << 5) | (((lane >> 5) & 1) << 8); }
; __device__ __forceinline__ void attn_body(const bf16_t* __restrict__ Qb, const bf16_t* __restrict__ Kh, const bf16_t* __restrict__ Vh, unsigned char* __restrict__ Ob, int ldo, int seq, LAS char* lds, const int wv, const float kbound, const float oscale) {
;   int tid = TIDX(wv); asm volatile("" : "+v"(tid));
;   const int wid = tid >> 6, lane = tid & 63, r32 = lane & 31, hi = lane >> 5;
;   LAS char* V_lds = lds; LAS char* K_lds = lds + 3 * SHM_V;
;   LAS float* ws = (LAS float*)(lds + 3 * SHM_V + 3 * SHM_K) + wid * 64; LAS float* li_l = ws; LAS float* al_l = ws + 32;
;   float l_reg = 0; f32x16 o[2] = {}; bf16x8 qr[DQK / 16];
;   const bf16_t* Qw = Qb + (long)(wid * QBLK + r32) * DQK + hi * 8;
; #pragma unroll
;   for (int d0 = 0; d0 < DQK / 16; ++d0) qr[d0] = *reinterpret_cast<const bf16x8*>(Qw + d0 * 16);
;   float nm;
;   { float qq = 0.f;
; #pragma unroll
;     for (int d0 = 0; d0 < DQK / 16; ++d0) { const u32x4 w = __builtin_bit_cast(u32x4, qr[d0]);
;       const float a0 = bf_lo(w.x), a1 = bf_hi(w.x), a2 = bf_lo(w.y), a3 = bf_hi(w.y), a4 = bf_lo(w.z), a5 = bf_hi(w.z), a6 = bf_lo(w.w), a7 = bf_hi(w.w);
;       qq += a0 * a0 + a1 * a1 + a2 * a2 + a3 * a3 + a4 * a4 + a5 * a5 + a6 * a6 + a7 * a7; }
;     { auto rr = __builtin_amdgcn_permlane32_swap(__float_as_uint(qq), __float_as_uint(qq), false, false); qq = __uint_as_float(rr[0]) + __uint_as_float(rr[1]); }
;     nm = -sqrtf(qq) * kbound * 1.01f; }
;   const int sr = tid >> 4, sc = (tid & 15) * 8;
;   const int vr = tid >> 3, vc = (tid & 7) * 8, vst0 = v_st(vr, vc);
;   const int vb0 = (int)(uintptr_t)V_lds + v_rd_base(lane);
;   struct { bf16x8 vs0, ks0, ks1; } sr_;
;     ...
;   f32x16 pA0, pA1, pB0, pB1; bf16x8 pa0, pa1, pa2, pa3; const int NT = seq / KVBLK;
;   SLOAD(0); SWRITE(0); SLOAD(KVBLK); SWRITE(1); SLOAD(2 * KVBLK); SWRITE(2); __syncthreads();
.LBB0_602:
	s_lshr_b32 s68, s14, 4
	s_lshl_b32 s16, s67, 15
	s_lshl_b32 s17, s68, 12
	s_lshl_b32 s4, s14, 8
	s_or_b32 s6, s17, s16
	s_and_b32 s69, s4, 0xf00
	s_or_b32 s4, s6, s69
	s_mulk_i32 s4, 0xc0
	s_add_u32 s4, s36, s4
	v_mbcnt_lo_u32_b32 v0, -1, 0
	v_mbcnt_hi_u32_b32 v0, -1, v0
	s_addc_u32 s5, s37, 0
	v_or_b32_e32 v173, s19, v0
	v_mov_b64_e32 v[0:1], s[4:5]
	v_ashrrev_i32_e32 v54, 1, v173
	v_bfe_u32 v186, v173, 5, 1
	v_bfi_b32 v2, s43, v54, v173
	v_mad_i64_i32 v[0:1], s[4:5], v2, s25, v[0:1]
	v_lshlrev_b32_e32 v170, 4, v186
	v_mov_b32_e32 v171, v169
	v_lshl_add_u64 v[0:1], v[0:1], 0, v[170:171]
	global_load_dwordx4 v[128:131], v[0:1], off
	global_load_dwordx4 v[132:135], v[0:1], off offset:32
	global_load_dwordx4 v[136:139], v[0:1], off offset:64
	global_load_dwordx4 v[140:143], v[0:1], off offset:96
	global_load_dwordx4 v[144:147], v[0:1], off offset:160
	global_load_dwordx4 v[148:151], v[0:1], off offset:128
	s_lshl_b64 s[4:5], s[6:7], 8
	s_add_u32 s4, s38, s4
	s_addc_u32 s5, s39, s5
	s_lshl_b64 s[14:15], s[6:7], 7
	v_ashrrev_i32_e32 v42, 3, v173
	s_add_u32 s14, s40, s14
	v_lshlrev_b32_e32 v56, 3, v173
	v_ashrrev_i32_e32 v43, 31, v42
	s_addc_u32 s15, s41, s15
	v_ashrrev_i32_e32 v40, 4, v173
	v_ashrrev_i32_e32 v41, 31, v40
	v_lshlrev_b32_e32 v64, 4, v173
	v_and_b32_e32 v46, 0xf0, v64
	v_mov_b32_e32 v47, v169
	v_add_u32_e32 v50, 32, v40
	v_ashrrev_i32_e32 v51, 31, v50
	v_and_b32_e32 v168, 31, v173
	v_lshlrev_b32_e32 v192, 8, v168
	v_add_u32_e32 v193, 0, v192
	v_bitop3_b32 v198, v170, v64, s46 bitop3:0x78
	v_and_b32_e32 v171, 63, v173
	s_mov_b32 s70, 1
	v_and_b32_e32 v172, 0xffffffe0, v54
	v_mov_b32_e32 v187, 0
	s_mov_b32 s71, 0
	s_waitcnt vmcnt(5)
	v_and_b32_e32 v1, 0xffff0000, v128
	s_waitcnt vmcnt(4)
	v_and_b32_e32 v9, 0xffff0000, v132
	v_lshlrev_b32_e32 v0, 16, v128
	v_lshlrev_b32_e32 v8, 16, v132
	s_waitcnt vmcnt(3)
	v_and_b32_e32 v17, 0xffff0000, v136
	v_mul_f32_e32 v1, v1, v1
	v_mul_f32_e32 v9, v9, v9
	v_lshlrev_b32_e32 v2, 16, v129
	v_lshlrev_b32_e32 v10, 16, v133
	v_lshlrev_b32_e32 v16, 16, v136
	s_waitcnt vmcnt(2)
	v_and_b32_e32 v25, 0xffff0000, v140
	v_mul_f32_e32 v17, v17, v17
	v_fmac_f32_e32 v1, v0, v0
	v_fmac_f32_e32 v9, v8, v8
	v_and_b32_e32 v3, 0xffff0000, v129
	v_and_b32_e32 v11, 0xffff0000, v133
	v_lshlrev_b32_e32 v18, 16, v137
	v_lshlrev_b32_e32 v24, 16, v140
	v_mul_f32_e32 v25, v25, v25
	v_fmac_f32_e32 v17, v16, v16
	v_fmac_f32_e32 v1, v2, v2
	v_fmac_f32_e32 v9, v10, v10
	v_lshlrev_b32_e32 v4, 16, v130
	v_lshlrev_b32_e32 v12, 16, v134
	v_and_b32_e32 v19, 0xffff0000, v137
	v_lshlrev_b32_e32 v26, 16, v141
	v_fmac_f32_e32 v25, v24, v24
	v_fmac_f32_e32 v17, v18, v18
	v_fmac_f32_e32 v1, v3, v3
	v_fmac_f32_e32 v9, v11, v11
	v_and_b32_e32 v5, 0xffff0000, v130
	v_and_b32_e32 v13, 0xffff0000, v134
	v_lshlrev_b32_e32 v20, 16, v138
	v_and_b32_e32 v27, 0xffff0000, v141
	v_fmac_f32_e32 v25, v26, v26
	v_fmac_f32_e32 v17, v19, v19
	v_fmac_f32_e32 v1, v4, v4
	v_fmac_f32_e32 v9, v12, v12
	v_lshlrev_b32_e32 v6, 16, v131
	v_lshlrev_b32_e32 v14, 16, v135
	v_and_b32_e32 v21, 0xffff0000, v138
	v_lshlrev_b32_e32 v28, 16, v142
	v_fmac_f32_e32 v25, v27, v27
	v_fmac_f32_e32 v17, v20, v20
	v_fmac_f32_e32 v1, v5, v5
	v_fmac_f32_e32 v9, v13, v13
	v_and_b32_e32 v7, 0xffff0000, v131
	v_and_b32_e32 v15, 0xffff0000, v135
	v_lshlrev_b32_e32 v22, 16, v139
	v_and_b32_e32 v29, 0xffff0000, v142
	v_fmac_f32_e32 v25, v28, v28
	v_fmac_f32_e32 v17, v21, v21
	v_fmac_f32_e32 v1, v6, v6
	v_fmac_f32_e32 v9, v14, v14
	v_and_b32_e32 v23, 0xffff0000, v139
	v_lshlrev_b32_e32 v30, 16, v143
	v_fmac_f32_e32 v25, v29, v29
	v_fmac_f32_e32 v17, v22, v22
	v_fmac_f32_e32 v1, v7, v7
	v_fmac_f32_e32 v9, v15, v15
	v_and_b32_e32 v31, 0xffff0000, v143
	v_fmac_f32_e32 v25, v30, v30
	v_fmac_f32_e32 v17, v23, v23
	v_add_f32_e32 v0, v1, v9
	v_fmac_f32_e32 v25, v31, v31
	v_add_f32_e32 v0, v0, v17
	v_and_b32_e32 v2, 56, v56
	v_lshlrev_b64 v[16:17], 7, v[42:43]
	v_add_f32_e32 v55, v0, v25
	v_lshl_add_u64 v[0:1], s[14:15], 0, v[16:17]
	v_lshlrev_b32_e32 v2, 1, v2
	v_mov_b32_e32 v3, v169
	v_lshl_add_u64 v[44:45], v[0:1], 0, v[2:3]
	v_lshlrev_b64 v[18:19], 8, v[40:41]
	v_lshl_add_u64 v[0:1], s[4:5], 0, v[18:19]
	v_add_co_u32_e32 v12, vcc, s48, v44
	v_lshl_add_u64 v[48:49], v[0:1], 0, v[46:47]
	s_nop 0
	v_addc_co_u32_e32 v13, vcc, 0, v45, vcc
	v_add_co_u32_e32 v20, vcc, s49, v48
	global_load_dwordx4 v[0:3], v[44:45], off
	global_load_dwordx4 v[4:7], v[48:49], off
	v_addc_co_u32_e32 v21, vcc, 0, v49, vcc
	v_add_co_u32_e32 v24, vcc, s50, v48
	v_lshlrev_b64 v[8:9], 8, v[50:51]
	s_nop 0
	v_addc_co_u32_e32 v25, vcc, 0, v49, vcc
	v_add_co_u32_e32 v44, vcc, s49, v44
	v_lshl_add_u64 v[8:9], s[4:5], 0, v[8:9]
	s_nop 0
	v_addc_co_u32_e32 v45, vcc, 0, v45, vcc
	v_lshl_add_u64 v[8:9], v[8:9], 0, v[46:47]
	v_add_co_u32_e32 v52, vcc, s51, v48
	global_load_dwordx4 v[8:11], v[8:9], off
	s_nop 0
	global_load_dwordx4 v[12:15], v[12:13], off
	s_nop 0
	global_load_dwordx4 v[20:23], v[20:21], off
	s_nop 0
	global_load_dwordx4 v[24:27], v[24:25], off
	v_addc_co_u32_e32 v53, vcc, 0, v49, vcc
	global_load_dwordx4 v[152:155], v[44:45], off
	global_load_dwordx4 v[156:159], v[52:53], off
	v_add_co_u32_e32 v44, vcc, s57, v48
	s_waitcnt vmcnt(9)
	v_and_b32_e32 v31, 0xffff0000, v144
	v_addc_co_u32_e32 v45, vcc, 0, v49, vcc
	global_load_dwordx4 v[160:163], v[44:45], off
	s_waitcnt vmcnt(9)
; #define LAS __attribute__((address_space(3)))
; __device__ __forceinline__ int v_st(int k, int c) { const int kk = (k & ~0xC) | ((k & 4) << 1) | ((k & 8) >> 1); return ((kk >> 3) * 2 + (c >> 5)) * 512 + ((kk & 7) * 32 + (c & 31)) * 2; }
; __device__ __forceinline__ void qkt(f32x16& p0, f32x16& p1, const LAS char* Ks, const bf16x8* qr, int r32, int hi, float nm) {
; #pragma unroll
;   for (int r = 0; r < 16; ++r) { p0[r] = nm; p1[r] = nm; }
; #pragma unroll
;   for (int d0 = 0; d0 < DQK / 16; ++d0) { int cb = (d0 * 16 + hi * 8) * 2;
;     bf16x8 b0 = *reinterpret_cast<const LAS bf16x8*>(Ks + KSWZ(r32, cb));
;     bf16x8 b1 = *reinterpret_cast<const LAS bf16x8*>(Ks + KSWZ(32 + r32, cb));
;     __builtin_amdgcn_s_setprio(1);
;     p0 = __builtin_amdgcn_mfma_f32_32x32x16_bf16(b0, qr[d0], p0, 0, 0, 0);
;     p1 = __builtin_amdgcn_mfma_f32_32x32x16_bf16(b1, qr[d0], p1, 0, 0, 0);
;     __builtin_amdgcn_s_setprio(0); }
; __device__ __forceinline__ void attn_body(const bf16_t* __restrict__ Qb, const bf16_t* __restrict__ Kh, const bf16_t* __restrict__ Vh, unsigned char* __restrict__ Ob, int ldo, int seq, LAS char* lds, const int wv, const float kbound, const float oscale) {
;     ...
;   { float qq = 0.f;
; #pragma unroll
;     for (int d0 = 0; d0 < DQK / 16; ++d0) { const u32x4 w = __builtin_bit_cast(u32x4, qr[d0]);
;       const float a0 = bf_lo(w.x), a1 = bf_hi(w.x), a2 = bf_lo(w.y), a3 = bf_hi(w.y), a4 = bf_lo(w.z), a5 = bf_hi(w.z), a6 = bf_lo(w.w), a7 = bf_hi(w.w);
;       qq += a0 * a0 + a1 * a1 + a2 * a2 + a3 * a3 + a4 * a4 + a5 * a5 + a6 * a6 + a7 * a7; }
;     { auto rr = __builtin_amdgcn_permlane32_swap(__float_as_uint(qq), __float_as_uint(qq), false, false); qq = __uint_as_float(rr[0]) + __uint_as_float(rr[1]); }
;     nm = -sqrtf(qq) * kbound * 1.01f; }
;   const int sr = tid >> 4, sc = (tid & 15) * 8;
;   const int vr = tid >> 3, vc = (tid & 7) * 8, vst0 = v_st(vr, vc);
;   const int vb0 = (int)(uintptr_t)V_lds + v_rd_base(lane);
;   struct { bf16x8 vs0, ks0, ks1; } sr_;
;     ...
;   f32x16 pA0, pA1, pB0, pB1; bf16x8 pa0, pa1, pa2, pa3; const int NT = seq / KVBLK;
;   SLOAD(0); SWRITE(0); SLOAD(KVBLK); SWRITE(1); SLOAD(2 * KVBLK); SWRITE(2); __syncthreads();
;   qkt(pA0, pA1, K_lds, qr, r32, hi, nm); partialSM(pA0, pA1);
	v_and_b32_e32 v30, 0xffff0000, v148
	v_lshlrev_b32_e32 v29, 16, v144
	v_lshlrev_b32_e32 v28, 16, v148
	v_pk_mul_f32 v[30:31], v[30:31], v[30:31]
	v_lshlrev_b32_e32 v33, 16, v145
	v_lshlrev_b32_e32 v32, 16, v149
	v_pk_fma_f32 v[28:29], v[28:29], v[28:29], v[30:31]
	v_and_b32_e32 v35, 0xffff0000, v145
	v_and_b32_e32 v34, 0xffff0000, v149
	v_pk_fma_f32 v[28:29], v[32:33], v[32:33], v[28:29]
	v_lshlrev_b32_e32 v37, 16, v146
	v_lshlrev_b32_e32 v36, 16, v150
	v_pk_fma_f32 v[28:29], v[34:35], v[34:35], v[28:29]
	v_and_b32_e32 v39, 0xffff0000, v146
	v_and_b32_e32 v38, 0xffff0000, v150
	v_pk_fma_f32 v[28:29], v[36:37], v[36:37], v[28:29]
	v_lshlrev_b32_e32 v45, 16, v147
	v_lshlrev_b32_e32 v44, 16, v151
	v_pk_fma_f32 v[28:29], v[38:39], v[38:39], v[28:29]
	v_and_b32_e32 v49, 0xffff0000, v147
	v_and_b32_e32 v48, 0xffff0000, v151
	v_pk_fma_f32 v[28:29], v[44:45], v[44:45], v[28:29]
	s_nop 0
	v_pk_fma_f32 v[28:29], v[48:49], v[48:49], v[28:29]
	s_nop 0
	v_add_f32_e32 v28, v55, v28
	v_add_f32_e32 v28, v28, v29
	v_mov_b32_e32 v29, v28
	s_nop 1
	v_permlane32_swap_b32_e32 v28, v29
	v_add_f32_e32 v28, v28, v29
	v_mul_f32_e32 v29, 0x4f800000, v28
	v_cmp_gt_f32_e32 vcc, s44, v28
	s_nop 1
	v_cndmask_b32_e32 v28, v28, v29, vcc
	v_sqrt_f32_e32 v29, v28
	s_nop 0
	v_add_u32_e32 v30, -1, v29
	v_fma_f32 v31, -v30, v29, v28
	v_cmp_ge_f32_e64 s[4:5], 0, v31
	v_add_u32_e32 v31, 1, v29
	s_nop 0
	v_cndmask_b32_e64 v30, v29, v30, s[4:5]
	v_fma_f32 v29, -v31, v29, v28
	v_cmp_lt_f32_e64 s[4:5], 0, v29
	s_nop 1
	v_cndmask_b32_e64 v29, v30, v31, s[4:5]
	v_mul_f32_e32 v30, 0x37800000, v29
	v_cndmask_b32_e32 v29, v29, v30, vcc
	v_cmp_class_f32_e32 vcc, v28, v184
	v_bfe_u32 v30, v56, 5, 1
	v_lshlrev_b32_e32 v31, 1, v173
	v_cndmask_b32_e32 v28, v29, v28, vcc
	v_mul_f32_e32 v28, v183, v28
	v_mul_f32_e32 v32, 0xbf8147ae, v28
	v_and_b32_e32 v28, 0x1fffff0, v42
	v_lshlrev_b32_e32 v29, 1, v42
	v_and_or_b32 v28, v29, 8, v28
	v_lshrrev_b32_e32 v28, 2, v28
	v_lshrrev_b32_e32 v29, 1, v42
	v_or_b32_e32 v28, v28, v30
	v_and_b32_e32 v30, 3, v42
	v_and_or_b32 v29, v29, 4, v30
	v_and_b32_e32 v30, 48, v64
	v_lshl_or_b32 v29, v29, 6, v30
	v_lshl_or_b32 v28, v28, 9, v29
	v_add_u32_e32 v189, 0, v28
	s_waitcnt vmcnt(8)
	ds_write_b128 v189, v[0:3]
	v_lshlrev_b32_e32 v0, 8, v40
	v_and_b32_e32 v1, 0x70, v173
	v_lshlrev_b32_e32 v2, 8, v50
	v_bitop3_b32 v190, v46, v0, v1 bitop3:0xde
	v_bitop3_b32 v191, v46, v2, v1 bitop3:0xde
	v_add_u32_e32 v0, 0, v190
	v_add_u32_e32 v1, 0, v191
	s_waitcnt vmcnt(7)
	ds_write_b128 v0, v[4:7] offset:24576
	s_waitcnt vmcnt(6)
	ds_write_b128 v1, v[8:11] offset:24576
	s_waitcnt vmcnt(5)
	ds_write_b128 v189, v[12:15] offset:8192
	s_waitcnt vmcnt(4)
	ds_write_b128 v0, v[20:23] offset:40960
	s_waitcnt vmcnt(3)
	ds_write_b128 v1, v[24:27] offset:40960
	s_waitcnt vmcnt(2)
	ds_write_b128 v189, v[152:155] offset:16384
	s_waitcnt vmcnt(1)
	ds_write_b128 v0, v[156:159] offset:57344
	s_waitcnt vmcnt(0)
	ds_write_b128 v1, v[160:163] offset:57344
	v_add_u32_e32 v0, v193, v198
	s_waitcnt lgkmcnt(0)
	s_barrier
	ds_read_b128 v[20:23], v0 offset:24576
	ds_read_b128 v[24:27], v0 offset:32768
	v_lshlrev_b32_e32 v29, 3, v171
	v_and_b32_e32 v30, 0xc0, v64
	v_and_or_b32 v30, v29, 24, v30
	v_and_b32_e32 v31, 32, v31
	v_and_b32_e32 v29, 0x100, v29
	v_or3_b32 v29, v30, v31, v29
	s_mov_b32 s4, 2
	v_add_u32_e32 v188, 0, v29
	v_mov_b32_e32 v48, v32
	v_mov_b32_e32 v49, v32
	v_mov_b32_e32 v50, v32
	v_mov_b32_e32 v51, v32
	v_mov_b32_e32 v52, v32
	v_mov_b32_e32 v53, v32
	v_mov_b32_e32 v54, v32
	v_mov_b32_e32 v55, v32
	v_mov_b32_e32 v56, v32
	v_mov_b32_e32 v57, v32
	v_mov_b32_e32 v58, v32
	v_mov_b32_e32 v59, v32
	v_mov_b32_e32 v60, v32
	v_mov_b32_e32 v61, v32
	v_mov_b32_e32 v62, v32
	v_mov_b32_e32 v63, v32
	v_and_b32_e32 v28, 0x70, v64
	s_waitcnt lgkmcnt(1)
	v_mfma_f32_32x32x16_bf16 v[0:15], v[20:23], v[128:131], v[48:63]
	s_waitcnt lgkmcnt(0)
	v_mfma_f32_32x32x16_bf16 v[64:79], v[24:27], v[128:131], v[48:63]
	v_bitop3_b32 v199, v170, v28, 32 bitop3:0x36
	v_add_u32_e32 v24, v193, v199
	ds_read_b128 v[20:23], v24 offset:24576
	ds_read_b128 v[24:27], v24 offset:32768
	s_waitcnt lgkmcnt(1)
	v_mfma_f32_32x32x16_bf16 v[0:15], v[20:23], v[132:135], v[0:15]
	s_waitcnt lgkmcnt(0)
	v_mfma_f32_32x32x16_bf16 v[64:79], v[24:27], v[132:135], v[64:79]
	v_bitop3_b32 v200, v170, v28, 64 bitop3:0x36
	v_add_u32_e32 v24, v193, v200
	ds_read_b128 v[20:23], v24 offset:24576
	ds_read_b128 v[24:27], v24 offset:32768
	s_waitcnt lgkmcnt(1)
	v_mfma_f32_32x32x16_bf16 v[0:15], v[20:23], v[136:139], v[0:15]
	s_waitcnt lgkmcnt(0)
	v_mfma_f32_32x32x16_bf16 v[64:79], v[24:27], v[136:139], v[64:79]
	v_bitop3_b32 v201, v170, v28, s58 bitop3:0x36
	v_add_u32_e32 v24, v193, v201
	ds_read_b128 v[20:23], v24 offset:24576
	ds_read_b128 v[24:27], v24 offset:32768
	s_waitcnt lgkmcnt(1)
	v_mfma_f32_32x32x16_bf16 v[0:15], v[20:23], v[140:143], v[0:15]
	s_waitcnt lgkmcnt(0)
	v_mfma_f32_32x32x16_bf16 v[64:79], v[24:27], v[140:143], v[64:79]
	v_bitop3_b32 v202, v170, v28, s24 bitop3:0x36
	v_add_u32_e32 v24, v193, v202
	ds_read_b128 v[20:23], v24 offset:24576
	ds_read_b128 v[24:27], v24 offset:32768
	s_waitcnt lgkmcnt(1)
	v_mfma_f32_32x32x16_bf16 v[0:15], v[20:23], v[148:151], v[0:15]
	s_waitcnt lgkmcnt(0)
	v_mfma_f32_32x32x16_bf16 v[64:79], v[24:27], v[148:151], v[64:79]
	v_bitop3_b32 v203, v170, v28, s59 bitop3:0x36
	v_add_u32_e32 v24, v193, v203
	ds_read_b128 v[20:23], v24 offset:24576
	ds_read_b128 v[24:27], v24 offset:32768
	s_waitcnt lgkmcnt(1)
	v_mfma_f32_32x32x16_bf16 v[0:15], v[20:23], v[144:147], v[0:15]
	s_waitcnt lgkmcnt(0)
; #define LAS __attribute__((address_space(3)))
; #define SBAR() __builtin_amdgcn_sched_barrier(0)
; #define SLOAD(k0) do { sr_.vs0 = *reinterpret_cast<const bf16x8*>(&Vh[(long)((k0) + vr) * DVV + vc]); \
;     sr_.ks0 = *reinterpret_cast<const bf16x8*>(&Kh[(long)((k0) + sr) * KROW + sc]); sr_.ks1 = *reinterpret_cast<const bf16x8*>(&Kh[(long)((k0) + 32 + sr) * KROW + sc]); } while (0)
; __device__ __forceinline__ void finishSM(f32x16& p0, f32x16& p1, float& l_reg, bf16x8& pa0, bf16x8& pa1, bf16x8& pa2, bf16x8& pa3) {
;   for (int r = 0; r < 16; ++r) p1[r] = __builtin_amdgcn_exp2f(p1[r]);
;   float ps = 0; for (int r = 0; r < 16; ++r) ps += p0[r]; for (int r = 0; r < 16; ++r) ps += p1[r];
;   { auto rr = __builtin_amdgcn_permlane32_swap(__float_as_uint(ps), __float_as_uint(ps), false, false);
;     ps = __uint_as_float(rr[0]) + __uint_as_float(rr[1]); }
;   l_reg += ps;
;     ...
;   PK4(p0, 0, pa0); PK4(p0, 8, pa1); PK4(p1, 0, pa2); PK4(p1, 8, pa3);
;     ...
; }
; __device__ __forceinline__ void qkt(f32x16& p0, f32x16& p1, const LAS char* Ks, const bf16x8* qr, int r32, int hi, float nm) {
; #pragma unroll
;   for (int r = 0; r < 16; ++r) { p0[r] = nm; p1[r] = nm; }
; #pragma unroll
;   for (int d0 = 0; d0 < DQK / 16; ++d0) { int cb = (d0 * 16 + hi * 8) * 2;
;     bf16x8 b0 = *reinterpret_cast<const LAS bf16x8*>(Ks + KSWZ(r32, cb));
;     bf16x8 b1 = *reinterpret_cast<const LAS bf16x8*>(Ks + KSWZ(32 + r32, cb));
;     __builtin_amdgcn_s_setprio(1);
;     p0 = __builtin_amdgcn_mfma_f32_32x32x16_bf16(b0, qr[d0], p0, 0, 0, 0);
;     p1 = __builtin_amdgcn_mfma_f32_32x32x16_bf16(b1, qr[d0], p1, 0, 0, 0);
;     __builtin_amdgcn_s_setprio(0); }
; }
; __device__ __forceinline__ void attn_body(const bf16_t* __restrict__ Qb, const bf16_t* __restrict__ Kh, const bf16_t* __restrict__ Vh, unsigned char* __restrict__ Ob, int ldo, int seq, LAS char* lds, const int wv, const float kbound, const float oscale) {
;     ...
;   SLOAD(0); SWRITE(0); SLOAD(KVBLK); SWRITE(1); SLOAD(2 * KVBLK); SWRITE(2); __syncthreads();
;   qkt(pA0, pA1, K_lds, qr, r32, hi, nm); partialSM(pA0, pA1);
;   int b0 = 0, b1 = 1, b2 = 2;
; #pragma unroll 1
;   for (int j = 0; j < NT; j += 2) {
;     SBAR(); qkt(pB0, pB1, K_lds + b1 * SHM_K, qr, r32, hi, nm);
;     finishSM(pA0, pA1, l_reg, pa0, pa1, pa2, pa3); SBAR();
;     if (j + 3 < NT) SLOAD((j + 3) * KVBLK); SBAR();
	v_mfma_f32_32x32x16_bf16 v[64:79], v[24:27], v[144:147], v[64:79]
	s_add_i32 s6, s16, s17
	s_nop 7
	v_exp_f32_e32 v80, v0
	v_exp_f32_e32 v81, v1
	v_exp_f32_e32 v82, v2
	v_exp_f32_e32 v83, v3
	v_exp_f32_e32 v84, v4
	v_exp_f32_e32 v85, v5
	v_exp_f32_e32 v86, v6
	v_exp_f32_e32 v87, v7
	v_exp_f32_e32 v88, v8
	v_exp_f32_e32 v89, v9
	v_exp_f32_e32 v90, v10
	v_exp_f32_e32 v91, v11
	v_exp_f32_e32 v92, v12
	v_exp_f32_e32 v93, v13
	v_exp_f32_e32 v94, v14
	v_exp_f32_e32 v95, v15
	s_lshl_b64 s[14:15], s[6:7], 8
	v_lshl_add_u64 v[174:175], v[18:19], 0, s[14:15]
	v_and_b32_e32 v0, 15, v173
	s_lshl_b64 s[14:15], s[6:7], 7
	v_lshl_or_b32 v174, v0, 4, v174
	v_lshl_add_u64 v[176:177], v[16:17], 0, s[14:15]
	v_and_b32_e32 v0, 7, v173
	v_lshl_or_b32 v176, v0, 4, v176
	s_mov_b32 s6, 0
	v_mov_b32_e32 v0, 0
	v_mov_b32_e32 v1, v187
	v_mov_b32_e32 v2, v187
	v_mov_b32_e32 v3, v187
	v_mov_b32_e32 v4, v187
	v_mov_b32_e32 v5, v187
	v_mov_b32_e32 v6, v187
	v_mov_b32_e32 v7, v187
	v_mov_b32_e32 v8, v187
	v_mov_b32_e32 v9, v187
	v_mov_b32_e32 v10, v187
	v_mov_b32_e32 v11, v187
	v_mov_b32_e32 v12, v187
	v_mov_b32_e32 v13, v187
	v_mov_b32_e32 v14, v187
	v_mov_b32_e32 v15, v187
	v_mov_b32_e32 v16, 0
	v_mov_b32_e32 v17, v187
	v_mov_b32_e32 v18, v187
	v_mov_b32_e32 v19, v187
	v_mov_b32_e32 v20, v187
	v_mov_b32_e32 v21, v187
	v_mov_b32_e32 v22, v187
	v_mov_b32_e32 v23, v187
	v_mov_b32_e32 v24, v187
	v_mov_b32_e32 v25, v187
	v_mov_b32_e32 v26, v187
	v_mov_b32_e32 v27, v187
	v_mov_b32_e32 v28, v187
	v_mov_b32_e32 v29, v187
	v_mov_b32_e32 v30, v187
	v_mov_b32_e32 v31, v187
.LBB0_603:
	s_mov_b32 s72, s4
	s_lshl_b32 s4, s70, 14
	s_add_i32 s73, s4, 0
	v_add_u32_e32 v242, s73, v192
	v_add_u32_e32 v238, v242, v198
	ds_read_b128 v[234:237], v238 offset:24576
	ds_read_b128 v[238:241], v238 offset:32768
	v_add_f32_e32 v33, 0, v80
	v_add_f32_e32 v33, v81, v33
	v_add_f32_e32 v33, v82, v33
	v_add_f32_e32 v33, v83, v33
	v_add_f32_e32 v33, v84, v33
	s_waitcnt lgkmcnt(1)
	v_mfma_f32_32x32x16_bf16 v[112:127], v[234:237], v[128:131], v[48:63]
	v_add_f32_e32 v33, v85, v33
	v_add_f32_e32 v33, v86, v33
	v_add_f32_e32 v33, v87, v33
	v_add_f32_e32 v33, v88, v33
	s_waitcnt lgkmcnt(0)
	v_mfma_f32_32x32x16_bf16 v[96:111], v[238:241], v[128:131], v[48:63]
	v_add_f32_e32 v33, v89, v33
	v_add_f32_e32 v33, v90, v33
	v_add_f32_e32 v33, v91, v33
	v_add_u32_e32 v238, v242, v199
	ds_read_b128 v[234:237], v238 offset:24576
	ds_read_b128 v[238:241], v238 offset:32768
	v_exp_f32_e32 v64, v64
	v_add_f32_e32 v33, v92, v33
	v_exp_f32_e32 v65, v65
	v_add_f32_e32 v33, v93, v33
	v_exp_f32_e32 v66, v66
	s_waitcnt lgkmcnt(1)
	v_mfma_f32_32x32x16_bf16 v[112:127], v[234:237], v[132:135], v[112:127]
	v_add_f32_e32 v33, v94, v33
	v_exp_f32_e32 v67, v67
	v_add_f32_e32 v33, v95, v33
	v_exp_f32_e32 v68, v68
	s_waitcnt lgkmcnt(0)
	v_mfma_f32_32x32x16_bf16 v[96:111], v[238:241], v[132:135], v[96:111]
	v_add_f32_e32 v33, v64, v33
	v_exp_f32_e32 v69, v69
	v_add_f32_e32 v33, v65, v33
	v_add_u32_e32 v238, v242, v200
	ds_read_b128 v[234:237], v238 offset:24576
	ds_read_b128 v[238:241], v238 offset:32768
	v_exp_f32_e32 v70, v70
	v_add_f32_e32 v33, v66, v33
	v_exp_f32_e32 v71, v71
	v_add_f32_e32 v33, v67, v33
	v_exp_f32_e32 v72, v72
	s_waitcnt lgkmcnt(1)
	v_mfma_f32_32x32x16_bf16 v[112:127], v[234:237], v[136:139], v[112:127]
	v_add_f32_e32 v33, v68, v33
	v_exp_f32_e32 v73, v73
	v_add_f32_e32 v33, v69, v33
	v_exp_f32_e32 v74, v74
	s_waitcnt lgkmcnt(0)
	v_mfma_f32_32x32x16_bf16 v[96:111], v[238:241], v[136:139], v[96:111]
	v_add_f32_e32 v33, v70, v33
	v_exp_f32_e32 v75, v75
	v_add_f32_e32 v33, v71, v33
	v_add_u32_e32 v238, v242, v201
	ds_read_b128 v[234:237], v238 offset:24576
	ds_read_b128 v[238:241], v238 offset:32768
	v_exp_f32_e32 v76, v76
	v_add_f32_e32 v33, v72, v33
	v_exp_f32_e32 v77, v77
	v_add_f32_e32 v33, v73, v33
	v_exp_f32_e32 v78, v78
	s_waitcnt lgkmcnt(1)
	v_mfma_f32_32x32x16_bf16 v[112:127], v[234:237], v[140:143], v[112:127]
	v_add_f32_e32 v33, v74, v33
	v_exp_f32_e32 v79, v79
	v_add_f32_e32 v33, v75, v33
	v_add_f32_e32 v33, v76, v33
	s_waitcnt lgkmcnt(0)
	v_mfma_f32_32x32x16_bf16 v[96:111], v[238:241], v[140:143], v[96:111]
	v_add_f32_e32 v33, v77, v33
	v_add_f32_e32 v33, v78, v33
	v_add_f32_e32 v204, v79, v33
	v_add_u32_e32 v238, v242, v202
	ds_read_b128 v[234:237], v238 offset:24576
	ds_read_b128 v[238:241], v238 offset:32768
	v_mov_b32_e32 v205, v204
	v_cvt_pk_bf16_f32 v34, v80, v81
	v_cvt_pk_bf16_f32 v35, v82, v83
	v_cvt_pk_bf16_f32 v36, v84, v85
	v_cvt_pk_bf16_f32 v37, v86, v87
	s_waitcnt lgkmcnt(1)
	v_mfma_f32_32x32x16_bf16 v[112:127], v[234:237], v[148:151], v[112:127]
	v_cvt_pk_bf16_f32 v38, v88, v89
	v_cvt_pk_bf16_f32 v39, v90, v91
	v_cvt_pk_bf16_f32 v40, v92, v93
	v_cvt_pk_bf16_f32 v41, v94, v95
	s_waitcnt lgkmcnt(0)
	v_mfma_f32_32x32x16_bf16 v[96:111], v[238:241], v[148:151], v[96:111]
	v_cvt_pk_bf16_f32 v42, v64, v65
	v_cvt_pk_bf16_f32 v43, v66, v67
	v_cvt_pk_bf16_f32 v44, v68, v69
	v_add_u32_e32 v242, v242, v203
	ds_read_b128 v[234:237], v242 offset:24576
	ds_read_b128 v[238:241], v242 offset:32768
	v_cvt_pk_bf16_f32 v45, v70, v71
	v_cvt_pk_bf16_f32 v164, v72, v73
	v_cvt_pk_bf16_f32 v165, v74, v75
	v_cvt_pk_bf16_f32 v166, v76, v77
	v_cvt_pk_bf16_f32 v167, v78, v79
	s_waitcnt lgkmcnt(1)
	v_mfma_f32_32x32x16_bf16 v[112:127], v[234:237], v[144:147], v[112:127]
	s_nop 1
	v_permlane32_swap_b32_e32 v204, v205
	v_permlane32_swap_b32_e32 v34, v36
	v_permlane32_swap_b32_e32 v35, v37
	s_waitcnt lgkmcnt(0)
	v_mfma_f32_32x32x16_bf16 v[96:111], v[238:241], v[144:147], v[96:111]
	v_permlane32_swap_b32_e32 v38, v40
	v_permlane32_swap_b32_e32 v39, v41
	v_permlane32_swap_b32_e32 v42, v44
	v_permlane32_swap_b32_e32 v43, v45
	v_permlane32_swap_b32_e32 v164, v166
	v_permlane32_swap_b32_e32 v165, v167
	s_cmp_lt_u32 s71, 61
	s_cselect_b64 s[4:5], -1, 0
	s_cmp_gt_u32 s71, 60
	v_lshl_add_u64 v[180:181], s[22:23], 0, v[176:177]
	v_lshl_add_u64 v[178:179], s[22:23], 0, v[174:175]
	s_cbranch_scc1 .LBB0_605
	v_add_co_u32_e32 v46, vcc, 0x66006000, v180
	s_nop 1
	v_addc_co_u32_e32 v47, vcc, 0, v181, vcc
	s_waitcnt vmcnt(1)
	v_add_co_u32_e32 v156, vcc, 0x6200c000, v178
	s_nop 1
	v_addc_co_u32_e32 v157, vcc, 0, v179, vcc
	global_load_dwordx4 v[152:155], v[46:47], off
	s_nop 0
	global_load_dwordx4 v[156:159], v[156:157], off
	v_add_co_u32_e32 v46, vcc, 0x6200e000, v178
	s_nop 1
	v_addc_co_u32_e32 v47, vcc, 0, v179, vcc
	global_load_dwordx4 v[160:163], v[46:47], off
; #define SBAR() __builtin_amdgcn_sched_barrier(0)
; #define SWRITE(b) do { *(LAS bf16x8*)(V_lds + (b) * SHM_V + vst0) = sr_.vs0; int kc = sc * 2;               \
;     *(LAS bf16x8*)(K_lds + (b) * SHM_K + KSWZ(sr, kc)) = sr_.ks0;                       \
;     *(LAS bf16x8*)(K_lds + (b) * SHM_K + KSWZ(32 + sr, kc)) = sr_.ks1; } while (0)
; template <int D0> __device__ __forceinline__ void pv_one(f32x16& od, int vb, bf16x8 pa0, bf16x8 pa1, bf16x8 pa2, bf16x8 pa3) {
;   const s16x4 l0 = tr_read<v_rd_off(D0, 0, 0)>(vb), h0 = tr_read<v_rd_off(D0, 0, 1)>(vb), l1 = tr_read<v_rd_off(D0, 1, 0)>(vb), h1 = tr_read<v_rd_off(D0, 1, 1)>(vb);
;   const s16x4 l2 = tr_read<v_rd_off(D0, 2, 0)>(vb), h2 = tr_read<v_rd_off(D0, 2, 1)>(vb), l3 = tr_read<v_rd_off(D0, 3, 0)>(vb), h3 = tr_read<v_rd_off(D0, 3, 1)>(vb);
;   asm volatile("s_waitcnt lgkmcnt(0)" ::: "memory"); SBAR();
;     ...
;   __builtin_amdgcn_s_setprio(1);
;   od = __builtin_amdgcn_mfma_f32_32x32x16_bf16(pa0, PK(l0, h0), od, 0, 0, 0);
;   od = __builtin_amdgcn_mfma_f32_32x32x16_bf16(pa1, PK(l1, h1), od, 0, 0, 0);
;   od = __builtin_amdgcn_mfma_f32_32x32x16_bf16(pa2, PK(l2, h2), od, 0, 0, 0);
;   od = __builtin_amdgcn_mfma_f32_32x32x16_bf16(pa3, PK(l3, h3), od, 0, 0, 0);
;   __builtin_amdgcn_s_setprio(0);
;     ...
; }
; __device__ __forceinline__ void pv_d0(f32x16* o, int vb, bf16x8 pa0, bf16x8 pa1, bf16x8 pa2, bf16x8 pa3) {
;   pv_one<0>(o[0], vb, pa0, pa1, pa2, pa3); pv_one<1>(o[1], vb, pa0, pa1, pa2, pa3);
; __device__ __forceinline__ void attn_body(const bf16_t* __restrict__ Qb, const bf16_t* __restrict__ Kh, const bf16_t* __restrict__ Vh, unsigned char* __restrict__ Ob, int ldo, int seq, LAS char* lds, const int wv, const float kbound, const float oscale) {
;     ...
;     pv_d0(o, vb0 + b0 * (int)SHM_V, pa0, pa1, pa2, pa3); partialSM(pB0, pB1);
;     __syncthreads();
;     if (j + 3 < NT) SWRITE(b0);
;     SBAR(); if (j + 2 < NT) qkt(pA0, pA1, K_lds + b2 * SHM_K, qr, r32, hi, nm);
;     finishSM(pB0, pB1, l_reg, pa0, pa1, pa2, pa3); SBAR();
.LBB0_605:
	s_lshl_b32 s14, s6, 13
	v_add_u32_e32 v33, s14, v188
	ds_read_b64_tr_b16 v[206:207], v33 offset:0
	ds_read_b64_tr_b16 v[208:209], v33 offset:0x400
	ds_read_b64_tr_b16 v[210:211], v33 offset:0x800
	ds_read_b64_tr_b16 v[212:213], v33 offset:0xc00
	ds_read_b64_tr_b16 v[214:215], v33 offset:0x1000
	ds_read_b64_tr_b16 v[216:217], v33 offset:0x1400
	ds_read_b64_tr_b16 v[218:219], v33 offset:0x1800
	ds_read_b64_tr_b16 v[220:221], v33 offset:0x1c00
	s_waitcnt lgkmcnt(0)
	v_mfma_f32_32x32x16_bf16 v[0:15], v[34:37], v[206:209], v[0:15]
	v_mfma_f32_32x32x16_bf16 v[0:15], v[38:41], v[210:213], v[0:15]
	v_mfma_f32_32x32x16_bf16 v[0:15], v[42:45], v[214:217], v[0:15]
	v_mfma_f32_32x32x16_bf16 v[0:15], v[164:167], v[218:221], v[0:15]
	ds_read_b64_tr_b16 v[206:207], v33 offset:0x200
	ds_read_b64_tr_b16 v[208:209], v33 offset:0x600
	ds_read_b64_tr_b16 v[210:211], v33 offset:0xa00
	ds_read_b64_tr_b16 v[212:213], v33 offset:0xe00
	ds_read_b64_tr_b16 v[214:215], v33 offset:0x1200
	ds_read_b64_tr_b16 v[216:217], v33 offset:0x1600
	ds_read_b64_tr_b16 v[218:219], v33 offset:0x1a00
	ds_read_b64_tr_b16 v[220:221], v33 offset:0x1e00
	s_waitcnt lgkmcnt(0)
	v_mfma_f32_32x32x16_bf16 v[16:31], v[34:37], v[206:209], v[16:31]
	v_mfma_f32_32x32x16_bf16 v[16:31], v[38:41], v[210:213], v[16:31]
	v_mfma_f32_32x32x16_bf16 v[16:31], v[42:45], v[214:217], v[16:31]
	v_mfma_f32_32x32x16_bf16 v[16:31], v[164:167], v[218:221], v[16:31]
	s_andn2_b64 vcc, exec, s[4:5]
	s_barrier
	s_cbranch_vccnz .LBB0_607
	s_lshl_b32 s4, s6, 14
	s_add_i32 s4, s4, 0
	v_add_u32_e32 v35, s14, v189
	v_add_u32_e32 v33, s4, v191
	v_add_u32_e32 v34, s4, v190
	s_waitcnt vmcnt(2)
	ds_write_b128 v35, v[152:155]
	s_waitcnt vmcnt(1)
	ds_write_b128 v34, v[156:159] offset:24576
	s_waitcnt vmcnt(0)
	ds_write_b128 v33, v[160:163] offset:24576
.LBB0_607:
	s_cmp_lt_u32 s71, 62
	s_cselect_b64 s[14:15], -1, 0
	s_cmp_gt_u32 s71, 61
	s_cselect_b64 s[4:5], -1, 0
	s_and_b64 vcc, exec, s[4:5]
	s_cbranch_vccnz .Lattn0_s2only
	v_lshl_add_u32 v243, s72, 14, v193
	v_add_u32_e32 v238, v243, v198
	ds_read_b128 v[234:237], v238 offset:24576
	ds_read_b128 v[238:241], v238 offset:32768
	v_exp_f32_e32 v34, v112
	v_exp_f32_e32 v35, v113
	v_exp_f32_e32 v36, v114
	v_exp_f32_e32 v37, v115
	v_exp_f32_e32 v38, v116
	v_add_f32_e32 v33, 0, v34
	v_exp_f32_e32 v39, v117
	s_waitcnt lgkmcnt(1)
	v_mfma_f32_32x32x16_bf16 v[80:95], v[234:237], v[128:131], v[48:63]
	v_add_f32_e32 v33, v35, v33
	v_exp_f32_e32 v40, v118
	v_add_f32_e32 v33, v36, v33
	v_exp_f32_e32 v41, v119
	v_add_f32_e32 v33, v37, v33
	s_waitcnt lgkmcnt(0)
	v_mfma_f32_32x32x16_bf16 v[64:79], v[238:241], v[128:131], v[48:63]
	v_exp_f32_e32 v42, v120
	v_add_f32_e32 v33, v38, v33
	v_exp_f32_e32 v43, v121
	v_add_f32_e32 v33, v39, v33
	v_add_u32_e32 v238, v243, v199
	ds_read_b128 v[234:237], v238 offset:24576
	ds_read_b128 v[238:241], v238 offset:32768
	v_exp_f32_e32 v44, v122
	v_add_f32_e32 v33, v40, v33
	v_exp_f32_e32 v45, v123
	v_add_f32_e32 v33, v41, v33
	v_exp_f32_e32 v47, v124
	v_add_f32_e32 v33, v42, v33
	v_exp_f32_e32 v112, v125
	s_waitcnt lgkmcnt(1)
	v_mfma_f32_32x32x16_bf16 v[80:95], v[234:237], v[132:135], v[80:95]
	v_add_f32_e32 v33, v43, v33
	v_exp_f32_e32 v113, v126
	v_add_f32_e32 v33, v44, v33
	v_exp_f32_e32 v114, v127
	v_add_f32_e32 v33, v45, v33
	s_waitcnt lgkmcnt(0)
	v_mfma_f32_32x32x16_bf16 v[64:79], v[238:241], v[132:135], v[64:79]
	v_exp_f32_e32 v96, v96
	v_add_f32_e32 v33, v47, v33
	v_exp_f32_e32 v97, v97
	v_add_f32_e32 v33, v112, v33
	v_add_u32_e32 v238, v243, v200
	ds_read_b128 v[234:237], v238 offset:24576
	ds_read_b128 v[238:241], v238 offset:32768
	v_exp_f32_e32 v98, v98
	v_add_f32_e32 v33, v113, v33
	v_exp_f32_e32 v99, v99
	v_add_f32_e32 v33, v114, v33
	v_exp_f32_e32 v100, v100
	v_add_f32_e32 v33, v96, v33
	v_exp_f32_e32 v101, v101
	s_waitcnt lgkmcnt(1)
	v_mfma_f32_32x32x16_bf16 v[80:95], v[234:237], v[136:139], v[80:95]
	v_add_f32_e32 v33, v97, v33
	v_exp_f32_e32 v102, v102
	v_add_f32_e32 v33, v98, v33
	v_exp_f32_e32 v103, v103
	v_add_f32_e32 v33, v99, v33
	s_waitcnt lgkmcnt(0)
	v_mfma_f32_32x32x16_bf16 v[64:79], v[238:241], v[136:139], v[64:79]
	v_exp_f32_e32 v104, v104
	v_add_f32_e32 v33, v100, v33
	v_exp_f32_e32 v105, v105
	v_add_f32_e32 v33, v101, v33
	v_add_u32_e32 v238, v243, v201
	ds_read_b128 v[234:237], v238 offset:24576
	ds_read_b128 v[238:241], v238 offset:32768
	v_exp_f32_e32 v106, v106
	v_add_f32_e32 v33, v102, v33
	v_exp_f32_e32 v107, v107
	v_add_f32_e32 v33, v103, v33
	v_exp_f32_e32 v108, v108
	v_add_f32_e32 v33, v104, v33
	v_exp_f32_e32 v109, v109
	s_waitcnt lgkmcnt(1)
	v_mfma_f32_32x32x16_bf16 v[80:95], v[234:237], v[140:143], v[80:95]
	v_add_f32_e32 v33, v105, v33
	v_exp_f32_e32 v110, v110
	v_add_f32_e32 v33, v106, v33
	v_exp_f32_e32 v111, v111
	v_add_f32_e32 v33, v107, v33
	s_waitcnt lgkmcnt(0)
	v_mfma_f32_32x32x16_bf16 v[64:79], v[238:241], v[140:143], v[64:79]
	v_add_f32_e32 v33, v108, v33
	v_add_f32_e32 v33, v109, v33
	v_add_f32_e32 v33, v110, v33
	v_add_f32_e32 v33, v111, v33
	v_add_u32_e32 v238, v243, v202
	ds_read_b128 v[234:237], v238 offset:24576
	ds_read_b128 v[238:241], v238 offset:32768
	v_mov_b32_e32 v46, v33
	v_cvt_pk_bf16_f32 v34, v34, v35
	v_cvt_pk_bf16_f32 v35, v36, v37
	v_cvt_pk_bf16_f32 v36, v38, v39
	v_cvt_pk_bf16_f32 v37, v40, v41
	v_cvt_pk_bf16_f32 v38, v42, v43
	v_cvt_pk_bf16_f32 v39, v44, v45
	s_waitcnt lgkmcnt(1)
	v_mfma_f32_32x32x16_bf16 v[80:95], v[234:237], v[148:151], v[80:95]
	v_cvt_pk_bf16_f32 v40, v47, v112
	v_cvt_pk_bf16_f32 v41, v113, v114
	v_cvt_pk_bf16_f32 v42, v96, v97
	v_cvt_pk_bf16_f32 v43, v98, v99
	v_cvt_pk_bf16_f32 v44, v100, v101
	s_waitcnt lgkmcnt(0)
	v_mfma_f32_32x32x16_bf16 v[64:79], v[238:241], v[148:151], v[64:79]
	v_cvt_pk_bf16_f32 v45, v102, v103
	v_cvt_pk_bf16_f32 v96, v104, v105
	v_cvt_pk_bf16_f32 v97, v106, v107
	v_cvt_pk_bf16_f32 v98, v108, v109
	v_add_u32_e32 v238, v243, v203
	ds_read_b128 v[234:237], v238 offset:24576
	ds_read_b128 v[238:241], v238 offset:32768
	v_cvt_pk_bf16_f32 v99, v110, v111
	s_nop 1
	v_permlane32_swap_b32_e32 v33, v46
	v_permlane32_swap_b32_e32 v34, v36
	v_permlane32_swap_b32_e32 v35, v37
	v_permlane32_swap_b32_e32 v38, v40
	v_permlane32_swap_b32_e32 v39, v41
	s_waitcnt lgkmcnt(1)
	v_mfma_f32_32x32x16_bf16 v[80:95], v[234:237], v[144:147], v[80:95]
	v_permlane32_swap_b32_e32 v42, v44
	v_permlane32_swap_b32_e32 v43, v45
	v_permlane32_swap_b32_e32 v96, v98
	v_permlane32_swap_b32_e32 v97, v99
	s_waitcnt lgkmcnt(0)
	v_mfma_f32_32x32x16_bf16 v[64:79], v[238:241], v[144:147], v[64:79]
	s_branch .Lattn0_join

; #define SBAR() __builtin_amdgcn_sched_barrier(0)
; template <int D0> __device__ __forceinline__ void pv_one(f32x16& od, int vb, bf16x8 pa0, bf16x8 pa1, bf16x8 pa2, bf16x8 pa3) {
;   const s16x4 l0 = tr_read<v_rd_off(D0, 0, 0)>(vb), h0 = tr_read<v_rd_off(D0, 0, 1)>(vb), l1 = tr_read<v_rd_off(D0, 1, 0)>(vb), h1 = tr_read<v_rd_off(D0, 1, 1)>(vb);
;   const s16x4 l2 = tr_read<v_rd_off(D0, 2, 0)>(vb), h2 = tr_read<v_rd_off(D0, 2, 1)>(vb), l3 = tr_read<v_rd_off(D0, 3, 0)>(vb), h3 = tr_read<v_rd_off(D0, 3, 1)>(vb);
;   asm volatile("s_waitcnt lgkmcnt(0)" ::: "memory"); SBAR();
;     ...
;   __builtin_amdgcn_s_setprio(1);
;   od = __builtin_amdgcn_mfma_f32_32x32x16_bf16(pa0, PK(l0, h0), od, 0, 0, 0);
;   od = __builtin_amdgcn_mfma_f32_32x32x16_bf16(pa1, PK(l1, h1), od, 0, 0, 0);
;   od = __builtin_amdgcn_mfma_f32_32x32x16_bf16(pa2, PK(l2, h2), od, 0, 0, 0);
;   od = __builtin_amdgcn_mfma_f32_32x32x16_bf16(pa3, PK(l3, h3), od, 0, 0, 0);
;   __builtin_amdgcn_s_setprio(0);
;     ...
; }
; __device__ __forceinline__ void attn_body(const bf16_t* __restrict__ Qb, const bf16_t* __restrict__ Kh, const bf16_t* __restrict__ Vh, unsigned char* __restrict__ Ob, int ldo, int seq, LAS char* lds, const int wv, const float kbound, const float oscale) {
;     ...
;     pv_d0(o, vb0 + b1 * (int)SHM_V, pa0, pa1, pa2, pa3); if (j + 2 < NT) partialSM(pA0, pA1);
;     __syncthreads();
.LBB0_611:
	s_lshl_b32 s74, s70, 13
	v_add_u32_e32 v47, s74, v188
	ds_read_b64_tr_b16 v[100:101], v47 offset:0
	ds_read_b64_tr_b16 v[102:103], v47 offset:0x400
	ds_read_b64_tr_b16 v[104:105], v47 offset:0x800
	ds_read_b64_tr_b16 v[106:107], v47 offset:0xc00
	ds_read_b64_tr_b16 v[108:109], v47 offset:0x1000
	ds_read_b64_tr_b16 v[110:111], v47 offset:0x1400
	ds_read_b64_tr_b16 v[112:113], v47 offset:0x1800
	ds_read_b64_tr_b16 v[114:115], v47 offset:0x1c00
	s_waitcnt lgkmcnt(0)
	v_mfma_f32_32x32x16_bf16 v[0:15], v[34:37], v[100:103], v[0:15]
	v_exp_f32_e32 v80, v80
	v_exp_f32_e32 v81, v81
	v_mfma_f32_32x32x16_bf16 v[0:15], v[38:41], v[104:107], v[0:15]
	v_exp_f32_e32 v82, v82
	v_exp_f32_e32 v83, v83
	v_mfma_f32_32x32x16_bf16 v[0:15], v[42:45], v[108:111], v[0:15]
	v_exp_f32_e32 v84, v84
	v_exp_f32_e32 v85, v85
	v_mfma_f32_32x32x16_bf16 v[0:15], v[96:99], v[112:115], v[0:15]
	v_exp_f32_e32 v86, v86
	v_exp_f32_e32 v87, v87
	ds_read_b64_tr_b16 v[100:101], v47 offset:0x200
	ds_read_b64_tr_b16 v[102:103], v47 offset:0x600
	ds_read_b64_tr_b16 v[104:105], v47 offset:0xa00
	ds_read_b64_tr_b16 v[106:107], v47 offset:0xe00
	ds_read_b64_tr_b16 v[108:109], v47 offset:0x1200
	ds_read_b64_tr_b16 v[110:111], v47 offset:0x1600
	ds_read_b64_tr_b16 v[112:113], v47 offset:0x1a00
	ds_read_b64_tr_b16 v[114:115], v47 offset:0x1e00
	s_waitcnt lgkmcnt(0)
	v_mfma_f32_32x32x16_bf16 v[16:31], v[34:37], v[100:103], v[16:31]
	v_exp_f32_e32 v88, v88
	v_exp_f32_e32 v89, v89
	v_mfma_f32_32x32x16_bf16 v[16:31], v[38:41], v[104:107], v[16:31]
	v_exp_f32_e32 v90, v90
	v_exp_f32_e32 v91, v91
	v_mfma_f32_32x32x16_bf16 v[16:31], v[42:45], v[108:111], v[16:31]
	v_exp_f32_e32 v92, v92
	v_exp_f32_e32 v93, v93
	v_mfma_f32_32x32x16_bf16 v[16:31], v[96:99], v[112:115], v[16:31]
	v_exp_f32_e32 v94, v94
	v_exp_f32_e32 v95, v95

; #define LAS __attribute__((address_space(3)))
; #define TIDX(wv) (((wv) << 6) | lane_id())
; __device__ __forceinline__ int v_st(int k, int c) { const int kk = (k & ~0xC) | ((k & 4) << 1) | ((k & 8) >> 1); return ((kk >> 3) * 2 + (c >> 5)) * 512 + ((kk & 7) * 32 + (c & 31)) * 2; }
; __device__ __forceinline__ int v_rd_base(int lane) { return ((lane & 3) << 3) | (((lane >> 2) & 3) << 6) | (((lane >> 4) & 1) << 5) | (((lane >> 5) & 1) << 8); }
; __device__ __forceinline__ void attn_body(const bf16_t* __restrict__ Qb, const bf16_t* __restrict__ Kh, const bf16_t* __restrict__ Vh, unsigned char* __restrict__ Ob, int ldo, int seq, LAS char* lds, const int wv, const float kbound, const float oscale) {
;   int tid = TIDX(wv); asm volatile("" : "+v"(tid));
;   const int wid = tid >> 6, lane = tid & 63, r32 = lane & 31, hi = lane >> 5;
;   LAS char* V_lds = lds; LAS char* K_lds = lds + 3 * SHM_V;
;   LAS float* ws = (LAS float*)(lds + 3 * SHM_V + 3 * SHM_K) + wid * 64; LAS float* li_l = ws; LAS float* al_l = ws + 32;
;   float l_reg = 0; f32x16 o[2] = {}; bf16x8 qr[DQK / 16];
;   const bf16_t* Qw = Qb + (long)(wid * QBLK + r32) * DQK + hi * 8;
; #pragma unroll
;   for (int d0 = 0; d0 < DQK / 16; ++d0) qr[d0] = *reinterpret_cast<const bf16x8*>(Qw + d0 * 16);
;   float nm;
;   { float qq = 0.f;
; #pragma unroll
;     for (int d0 = 0; d0 < DQK / 16; ++d0) { const u32x4 w = __builtin_bit_cast(u32x4, qr[d0]);
;       const float a0 = bf_lo(w.x), a1 = bf_hi(w.x), a2 = bf_lo(w.y), a3 = bf_hi(w.y), a4 = bf_lo(w.z), a5 = bf_hi(w.z), a6 = bf_lo(w.w), a7 = bf_hi(w.w);
;       qq += a0 * a0 + a1 * a1 + a2 * a2 + a3 * a3 + a4 * a4 + a5 * a5 + a6 * a6 + a7 * a7; }
;     { auto rr = __builtin_amdgcn_permlane32_swap(__float_as_uint(qq), __float_as_uint(qq), false, false); qq = __uint_as_float(rr[0]) + __uint_as_float(rr[1]); }
;     nm = -sqrtf(qq) * kbound * 1.01f; }
;   const int sr = tid >> 4, sc = (tid & 15) * 8;
;   const int vr = tid >> 3, vc = (tid & 7) * 8, vst0 = v_st(vr, vc);
;   const int vb0 = (int)(uintptr_t)V_lds + v_rd_base(lane);
;   struct { bf16x8 vs0, ks0, ks1; } sr_;
;     ...
;   f32x16 pA0, pA1, pB0, pB1; bf16x8 pa0, pa1, pa2, pa3; const int NT = seq / KVBLK;
;   SLOAD(0); SWRITE(0); SLOAD(KVBLK); SWRITE(1); SLOAD(2 * KVBLK); SWRITE(2); __syncthreads();
.LBB0_3143:
	s_lshr_b32 s70, s14, 4
	s_lshl_b32 s16, s69, 15
	s_lshl_b32 s17, s70, 12
	s_lshl_b32 s4, s14, 8
	s_or_b32 s6, s17, s16
	s_and_b32 s71, s4, 0xf00
	s_or_b32 s4, s6, s71
	s_mulk_i32 s4, 0xc0
	s_add_u32 s4, s38, s4
	v_mbcnt_lo_u32_b32 v0, -1, 0
	v_mbcnt_hi_u32_b32 v0, -1, v0
	s_addc_u32 s5, s39, 0
	v_or_b32_e32 v173, s19, v0
	v_mov_b64_e32 v[0:1], s[4:5]
	v_ashrrev_i32_e32 v54, 1, v173
	v_bfe_u32 v186, v173, 5, 1
	v_bfi_b32 v2, s46, v54, v173
	v_mad_i64_i32 v[0:1], s[4:5], v2, s25, v[0:1]
	v_lshlrev_b32_e32 v170, 4, v186
	v_mov_b32_e32 v171, v169
	v_lshl_add_u64 v[0:1], v[0:1], 0, v[170:171]
	global_load_dwordx4 v[128:131], v[0:1], off
	global_load_dwordx4 v[132:135], v[0:1], off offset:32
	global_load_dwordx4 v[136:139], v[0:1], off offset:64
	global_load_dwordx4 v[140:143], v[0:1], off offset:96
	global_load_dwordx4 v[144:147], v[0:1], off offset:160
	global_load_dwordx4 v[148:151], v[0:1], off offset:128
	s_lshl_b64 s[4:5], s[6:7], 8
	s_add_u32 s4, s40, s4
	s_addc_u32 s5, s41, s5
	s_lshl_b64 s[14:15], s[6:7], 7
	v_ashrrev_i32_e32 v42, 3, v173
	s_add_u32 s14, s42, s14
	v_lshlrev_b32_e32 v56, 3, v173
	v_ashrrev_i32_e32 v43, 31, v42
	s_addc_u32 s15, s43, s15
	v_ashrrev_i32_e32 v40, 4, v173
	v_ashrrev_i32_e32 v41, 31, v40
	v_lshlrev_b32_e32 v64, 4, v173
	v_and_b32_e32 v46, 0xf0, v64
	v_mov_b32_e32 v47, v169
	v_add_u32_e32 v50, 32, v40
	v_ashrrev_i32_e32 v51, 31, v50
	v_and_b32_e32 v168, 31, v173
	v_lshlrev_b32_e32 v192, 8, v168
	v_add_u32_e32 v193, 0, v192
	v_bitop3_b32 v198, v170, v64, s49 bitop3:0x78
	v_and_b32_e32 v171, 63, v173
	s_mov_b32 s72, 1
	v_and_b32_e32 v172, 0xffffffe0, v54
	v_mov_b32_e32 v187, 0
	s_mov_b32 s73, 0
	s_waitcnt vmcnt(5)
	v_and_b32_e32 v1, 0xffff0000, v128
	s_waitcnt vmcnt(4)
	v_and_b32_e32 v9, 0xffff0000, v132
	v_lshlrev_b32_e32 v0, 16, v128
	v_lshlrev_b32_e32 v8, 16, v132
	s_waitcnt vmcnt(3)
	v_and_b32_e32 v17, 0xffff0000, v136
	v_mul_f32_e32 v1, v1, v1
	v_mul_f32_e32 v9, v9, v9
	v_lshlrev_b32_e32 v2, 16, v129
	v_lshlrev_b32_e32 v10, 16, v133
	v_lshlrev_b32_e32 v16, 16, v136
	s_waitcnt vmcnt(2)
	v_and_b32_e32 v25, 0xffff0000, v140
	v_mul_f32_e32 v17, v17, v17
	v_fmac_f32_e32 v1, v0, v0
	v_fmac_f32_e32 v9, v8, v8
	v_and_b32_e32 v3, 0xffff0000, v129
	v_and_b32_e32 v11, 0xffff0000, v133
	v_lshlrev_b32_e32 v18, 16, v137
	v_lshlrev_b32_e32 v24, 16, v140
	v_mul_f32_e32 v25, v25, v25
	v_fmac_f32_e32 v17, v16, v16
	v_fmac_f32_e32 v1, v2, v2
	v_fmac_f32_e32 v9, v10, v10
	v_lshlrev_b32_e32 v4, 16, v130
	v_lshlrev_b32_e32 v12, 16, v134
	v_and_b32_e32 v19, 0xffff0000, v137
	v_lshlrev_b32_e32 v26, 16, v141
	v_fmac_f32_e32 v25, v24, v24
	v_fmac_f32_e32 v17, v18, v18
	v_fmac_f32_e32 v1, v3, v3
	v_fmac_f32_e32 v9, v11, v11
	v_and_b32_e32 v5, 0xffff0000, v130
	v_and_b32_e32 v13, 0xffff0000, v134
	v_lshlrev_b32_e32 v20, 16, v138
	v_and_b32_e32 v27, 0xffff0000, v141
	v_fmac_f32_e32 v25, v26, v26
	v_fmac_f32_e32 v17, v19, v19
	v_fmac_f32_e32 v1, v4, v4
	v_fmac_f32_e32 v9, v12, v12
	v_lshlrev_b32_e32 v6, 16, v131
	v_lshlrev_b32_e32 v14, 16, v135
	v_and_b32_e32 v21, 0xffff0000, v138
	v_lshlrev_b32_e32 v28, 16, v142
	v_fmac_f32_e32 v25, v27, v27
	v_fmac_f32_e32 v17, v20, v20
	v_fmac_f32_e32 v1, v5, v5
	v_fmac_f32_e32 v9, v13, v13
	v_and_b32_e32 v7, 0xffff0000, v131
	v_and_b32_e32 v15, 0xffff0000, v135
	v_lshlrev_b32_e32 v22, 16, v139
	v_and_b32_e32 v29, 0xffff0000, v142
	v_fmac_f32_e32 v25, v28, v28
	v_fmac_f32_e32 v17, v21, v21
	v_fmac_f32_e32 v1, v6, v6
	v_fmac_f32_e32 v9, v14, v14
	v_and_b32_e32 v23, 0xffff0000, v139
	v_lshlrev_b32_e32 v30, 16, v143
	v_fmac_f32_e32 v25, v29, v29
	v_fmac_f32_e32 v17, v22, v22
	v_fmac_f32_e32 v1, v7, v7
	v_fmac_f32_e32 v9, v15, v15
	v_and_b32_e32 v31, 0xffff0000, v143
	v_fmac_f32_e32 v25, v30, v30
	v_fmac_f32_e32 v17, v23, v23
	v_add_f32_e32 v0, v1, v9
	v_fmac_f32_e32 v25, v31, v31
	v_add_f32_e32 v0, v0, v17
	v_and_b32_e32 v2, 56, v56
	v_lshlrev_b64 v[16:17], 7, v[42:43]
	v_add_f32_e32 v55, v0, v25
	v_lshl_add_u64 v[0:1], s[14:15], 0, v[16:17]
	v_lshlrev_b32_e32 v2, 1, v2
	v_mov_b32_e32 v3, v169
	v_lshl_add_u64 v[44:45], v[0:1], 0, v[2:3]
	v_lshlrev_b64 v[18:19], 8, v[40:41]
	v_lshl_add_u64 v[0:1], s[4:5], 0, v[18:19]
	v_add_co_u32_e32 v12, vcc, s50, v44
	v_lshl_add_u64 v[48:49], v[0:1], 0, v[46:47]
	s_nop 0
	v_addc_co_u32_e32 v13, vcc, 0, v45, vcc
	v_add_co_u32_e32 v20, vcc, s51, v48
	global_load_dwordx4 v[0:3], v[44:45], off
	global_load_dwordx4 v[4:7], v[48:49], off
	v_addc_co_u32_e32 v21, vcc, 0, v49, vcc
	v_add_co_u32_e32 v24, vcc, s57, v48
	v_lshlrev_b64 v[8:9], 8, v[50:51]
	s_nop 0
	v_addc_co_u32_e32 v25, vcc, 0, v49, vcc
	v_add_co_u32_e32 v44, vcc, s51, v44
	v_lshl_add_u64 v[8:9], s[4:5], 0, v[8:9]
	s_nop 0
	v_addc_co_u32_e32 v45, vcc, 0, v45, vcc
	v_lshl_add_u64 v[8:9], v[8:9], 0, v[46:47]
	v_add_co_u32_e32 v52, vcc, s58, v48
	global_load_dwordx4 v[8:11], v[8:9], off
	s_nop 0
	global_load_dwordx4 v[12:15], v[12:13], off
	s_nop 0
	global_load_dwordx4 v[20:23], v[20:21], off
	s_nop 0
	global_load_dwordx4 v[24:27], v[24:25], off
	v_addc_co_u32_e32 v53, vcc, 0, v49, vcc
	global_load_dwordx4 v[152:155], v[44:45], off
	global_load_dwordx4 v[156:159], v[52:53], off
	v_add_co_u32_e32 v44, vcc, s59, v48
	s_waitcnt vmcnt(9)
	v_and_b32_e32 v31, 0xffff0000, v144
	v_addc_co_u32_e32 v45, vcc, 0, v49, vcc
	global_load_dwordx4 v[160:163], v[44:45], off
	s_waitcnt vmcnt(9)
; #define LAS __attribute__((address_space(3)))
; __device__ __forceinline__ int v_st(int k, int c) { const int kk = (k & ~0xC) | ((k & 4) << 1) | ((k & 8) >> 1); return ((kk >> 3) * 2 + (c >> 5)) * 512 + ((kk & 7) * 32 + (c & 31)) * 2; }
; __device__ __forceinline__ void qkt(f32x16& p0, f32x16& p1, const LAS char* Ks, const bf16x8* qr, int r32, int hi, float nm) {
; #pragma unroll
;   for (int r = 0; r < 16; ++r) { p0[r] = nm; p1[r] = nm; }
; #pragma unroll
;   for (int d0 = 0; d0 < DQK / 16; ++d0) { int cb = (d0 * 16 + hi * 8) * 2;
;     bf16x8 b0 = *reinterpret_cast<const LAS bf16x8*>(Ks + KSWZ(r32, cb));
;     bf16x8 b1 = *reinterpret_cast<const LAS bf16x8*>(Ks + KSWZ(32 + r32, cb));
;     __builtin_amdgcn_s_setprio(1);
;     p0 = __builtin_amdgcn_mfma_f32_32x32x16_bf16(b0, qr[d0], p0, 0, 0, 0);
;     p1 = __builtin_amdgcn_mfma_f32_32x32x16_bf16(b1, qr[d0], p1, 0, 0, 0);
;     __builtin_amdgcn_s_setprio(0); }
; }
; __device__ __forceinline__ void attn_body(const bf16_t* __restrict__ Qb, const bf16_t* __restrict__ Kh, const bf16_t* __restrict__ Vh, unsigned char* __restrict__ Ob, int ldo, int seq, LAS char* lds, const int wv, const float kbound, const float oscale) {
;     ...
;   float nm;
;   { float qq = 0.f;
; #pragma unroll
;     for (int d0 = 0; d0 < DQK / 16; ++d0) { const u32x4 w = __builtin_bit_cast(u32x4, qr[d0]);
;       const float a0 = bf_lo(w.x), a1 = bf_hi(w.x), a2 = bf_lo(w.y), a3 = bf_hi(w.y), a4 = bf_lo(w.z), a5 = bf_hi(w.z), a6 = bf_lo(w.w), a7 = bf_hi(w.w);
;       qq += a0 * a0 + a1 * a1 + a2 * a2 + a3 * a3 + a4 * a4 + a5 * a5 + a6 * a6 + a7 * a7; }
;     { auto rr = __builtin_amdgcn_permlane32_swap(__float_as_uint(qq), __float_as_uint(qq), false, false); qq = __uint_as_float(rr[0]) + __uint_as_float(rr[1]); }
;     nm = -sqrtf(qq) * kbound * 1.01f; }
;   const int sr = tid >> 4, sc = (tid & 15) * 8;
;   const int vr = tid >> 3, vc = (tid & 7) * 8, vst0 = v_st(vr, vc);
;   const int vb0 = (int)(uintptr_t)V_lds + v_rd_base(lane);
;   struct { bf16x8 vs0, ks0, ks1; } sr_;
;     ...
;   f32x16 pA0, pA1, pB0, pB1; bf16x8 pa0, pa1, pa2, pa3; const int NT = seq / KVBLK;
;   SLOAD(0); SWRITE(0); SLOAD(KVBLK); SWRITE(1); SLOAD(2 * KVBLK); SWRITE(2); __syncthreads();
;   qkt(pA0, pA1, K_lds, qr, r32, hi, nm); partialSM(pA0, pA1);
	v_and_b32_e32 v30, 0xffff0000, v148
	v_lshlrev_b32_e32 v29, 16, v144
	v_lshlrev_b32_e32 v28, 16, v148
	v_pk_mul_f32 v[30:31], v[30:31], v[30:31]
	v_lshlrev_b32_e32 v33, 16, v145
	v_lshlrev_b32_e32 v32, 16, v149
	v_pk_fma_f32 v[28:29], v[28:29], v[28:29], v[30:31]
	v_and_b32_e32 v35, 0xffff0000, v145
	v_and_b32_e32 v34, 0xffff0000, v149
	v_pk_fma_f32 v[28:29], v[32:33], v[32:33], v[28:29]
	v_lshlrev_b32_e32 v37, 16, v146
	v_lshlrev_b32_e32 v36, 16, v150
	v_pk_fma_f32 v[28:29], v[34:35], v[34:35], v[28:29]
	v_and_b32_e32 v39, 0xffff0000, v146
	v_and_b32_e32 v38, 0xffff0000, v150
	v_pk_fma_f32 v[28:29], v[36:37], v[36:37], v[28:29]
	v_lshlrev_b32_e32 v45, 16, v147
	v_lshlrev_b32_e32 v44, 16, v151
	v_pk_fma_f32 v[28:29], v[38:39], v[38:39], v[28:29]
	v_and_b32_e32 v49, 0xffff0000, v147
	v_and_b32_e32 v48, 0xffff0000, v151
	v_pk_fma_f32 v[28:29], v[44:45], v[44:45], v[28:29]
	s_nop 0
	v_pk_fma_f32 v[28:29], v[48:49], v[48:49], v[28:29]
	s_nop 0
	v_add_f32_e32 v28, v55, v28
	v_add_f32_e32 v28, v28, v29
	v_mov_b32_e32 v29, v28
	s_nop 1
	v_permlane32_swap_b32_e32 v28, v29
	v_add_f32_e32 v28, v28, v29
	v_mul_f32_e32 v29, 0x4f800000, v28
	v_cmp_gt_f32_e32 vcc, s48, v28
	s_nop 1
	v_cndmask_b32_e32 v28, v28, v29, vcc
	v_sqrt_f32_e32 v29, v28
	s_nop 0
	v_add_u32_e32 v30, -1, v29
	v_fma_f32 v31, -v30, v29, v28
	v_cmp_ge_f32_e64 s[4:5], 0, v31
	v_add_u32_e32 v31, 1, v29
	s_nop 0
	v_cndmask_b32_e64 v30, v29, v30, s[4:5]
	v_fma_f32 v29, -v31, v29, v28
	v_cmp_lt_f32_e64 s[4:5], 0, v29
	s_nop 1
	v_cndmask_b32_e64 v29, v30, v31, s[4:5]
	v_mul_f32_e32 v30, 0x37800000, v29
	v_cndmask_b32_e32 v29, v29, v30, vcc
	v_cmp_class_f32_e32 vcc, v28, v184
	v_bfe_u32 v30, v56, 5, 1
	v_lshlrev_b32_e32 v31, 1, v173
	v_cndmask_b32_e32 v28, v29, v28, vcc
	v_mul_f32_e32 v28, v183, v28
	v_mul_f32_e32 v32, 0xbf8147ae, v28
	v_and_b32_e32 v28, 0x1fffff0, v42
	v_lshlrev_b32_e32 v29, 1, v42
	v_and_or_b32 v28, v29, 8, v28
	v_lshrrev_b32_e32 v28, 2, v28
	v_lshrrev_b32_e32 v29, 1, v42
	v_or_b32_e32 v28, v28, v30
	v_and_b32_e32 v30, 3, v42
	v_and_or_b32 v29, v29, 4, v30
	v_and_b32_e32 v30, 48, v64
	v_lshl_or_b32 v29, v29, 6, v30
	v_lshl_or_b32 v28, v28, 9, v29
	v_add_u32_e32 v189, 0, v28
	s_waitcnt vmcnt(8)
	ds_write_b128 v189, v[0:3]
	v_lshlrev_b32_e32 v0, 8, v40
	v_and_b32_e32 v1, 0x70, v173
	v_lshlrev_b32_e32 v2, 8, v50
	v_bitop3_b32 v190, v46, v0, v1 bitop3:0xde
	v_bitop3_b32 v191, v46, v2, v1 bitop3:0xde
	v_add_u32_e32 v0, 0, v190
	v_add_u32_e32 v1, 0, v191
	s_waitcnt vmcnt(7)
	ds_write_b128 v0, v[4:7] offset:24576
	s_waitcnt vmcnt(6)
	ds_write_b128 v1, v[8:11] offset:24576
	s_waitcnt vmcnt(5)
	ds_write_b128 v189, v[12:15] offset:8192
	s_waitcnt vmcnt(4)
	ds_write_b128 v0, v[20:23] offset:40960
	s_waitcnt vmcnt(3)
	ds_write_b128 v1, v[24:27] offset:40960
	s_waitcnt vmcnt(2)
	ds_write_b128 v189, v[152:155] offset:16384
	s_waitcnt vmcnt(1)
	ds_write_b128 v0, v[156:159] offset:57344
	s_waitcnt vmcnt(0)
	ds_write_b128 v1, v[160:163] offset:57344
	v_add_u32_e32 v0, v193, v198
	s_waitcnt lgkmcnt(0)
	s_barrier
	ds_read_b128 v[20:23], v0 offset:24576
	ds_read_b128 v[24:27], v0 offset:32768
	v_lshlrev_b32_e32 v29, 3, v171
	v_and_b32_e32 v30, 0xc0, v64
	v_and_or_b32 v30, v29, 24, v30
	v_and_b32_e32 v31, 32, v31
	v_and_b32_e32 v29, 0x100, v29
	v_or3_b32 v29, v30, v31, v29
	s_mov_b32 s4, 2
	v_add_u32_e32 v188, 0, v29
	v_mov_b32_e32 v48, v32
	v_mov_b32_e32 v49, v32
	v_mov_b32_e32 v50, v32
	v_mov_b32_e32 v51, v32
	v_mov_b32_e32 v52, v32
	v_mov_b32_e32 v53, v32
	v_mov_b32_e32 v54, v32
	v_mov_b32_e32 v55, v32
	v_mov_b32_e32 v56, v32
	v_mov_b32_e32 v57, v32
	v_mov_b32_e32 v58, v32
	v_mov_b32_e32 v59, v32
	v_mov_b32_e32 v60, v32
	v_mov_b32_e32 v61, v32
	v_mov_b32_e32 v62, v32
	v_mov_b32_e32 v63, v32
	v_and_b32_e32 v28, 0x70, v64
	s_waitcnt lgkmcnt(1)
	v_mfma_f32_32x32x16_bf16 v[0:15], v[20:23], v[128:131], v[48:63]
	s_waitcnt lgkmcnt(0)
	v_mfma_f32_32x32x16_bf16 v[64:79], v[24:27], v[128:131], v[48:63]
	v_bitop3_b32 v199, v170, v28, 32 bitop3:0x36
	v_add_u32_e32 v24, v193, v199
	ds_read_b128 v[20:23], v24 offset:24576
	ds_read_b128 v[24:27], v24 offset:32768
	s_waitcnt lgkmcnt(1)
	v_mfma_f32_32x32x16_bf16 v[0:15], v[20:23], v[132:135], v[0:15]
	s_waitcnt lgkmcnt(0)
	v_mfma_f32_32x32x16_bf16 v[64:79], v[24:27], v[132:135], v[64:79]
	v_bitop3_b32 v200, v170, v28, 64 bitop3:0x36
	v_add_u32_e32 v24, v193, v200
	ds_read_b128 v[20:23], v24 offset:24576
	ds_read_b128 v[24:27], v24 offset:32768
	s_waitcnt lgkmcnt(1)
	v_mfma_f32_32x32x16_bf16 v[0:15], v[20:23], v[136:139], v[0:15]
	s_waitcnt lgkmcnt(0)
	v_mfma_f32_32x32x16_bf16 v[64:79], v[24:27], v[136:139], v[64:79]
	v_bitop3_b32 v201, v170, v28, s60 bitop3:0x36
	v_add_u32_e32 v24, v193, v201
	ds_read_b128 v[20:23], v24 offset:24576
	ds_read_b128 v[24:27], v24 offset:32768
	s_waitcnt lgkmcnt(1)
	v_mfma_f32_32x32x16_bf16 v[0:15], v[20:23], v[140:143], v[0:15]
	s_waitcnt lgkmcnt(0)
	v_mfma_f32_32x32x16_bf16 v[64:79], v[24:27], v[140:143], v[64:79]
	v_bitop3_b32 v202, v170, v28, s24 bitop3:0x36
	v_add_u32_e32 v24, v193, v202
	ds_read_b128 v[20:23], v24 offset:24576
	ds_read_b128 v[24:27], v24 offset:32768
	s_waitcnt lgkmcnt(1)
	v_mfma_f32_32x32x16_bf16 v[0:15], v[20:23], v[148:151], v[0:15]
	s_waitcnt lgkmcnt(0)
	v_mfma_f32_32x32x16_bf16 v[64:79], v[24:27], v[148:151], v[64:79]
	v_bitop3_b32 v203, v170, v28, s61 bitop3:0x36
	v_add_u32_e32 v24, v193, v203
	ds_read_b128 v[20:23], v24 offset:24576
	ds_read_b128 v[24:27], v24 offset:32768
	s_waitcnt lgkmcnt(1)
	v_mfma_f32_32x32x16_bf16 v[0:15], v[20:23], v[144:147], v[0:15]
	s_waitcnt lgkmcnt(0)
; #define LAS __attribute__((address_space(3)))
; #define SBAR() __builtin_amdgcn_sched_barrier(0)
; #define SLOAD(k0) do { sr_.vs0 = *reinterpret_cast<const bf16x8*>(&Vh[(long)((k0) + vr) * DVV + vc]); \
;     sr_.ks0 = *reinterpret_cast<const bf16x8*>(&Kh[(long)((k0) + sr) * KROW + sc]); sr_.ks1 = *reinterpret_cast<const bf16x8*>(&Kh[(long)((k0) + 32 + sr) * KROW + sc]); } while (0)
; __device__ __forceinline__ void finishSM(f32x16& p0, f32x16& p1, float& l_reg, bf16x8& pa0, bf16x8& pa1, bf16x8& pa2, bf16x8& pa3) {
;   for (int r = 0; r < 16; ++r) p1[r] = __builtin_amdgcn_exp2f(p1[r]);
;   float ps = 0; for (int r = 0; r < 16; ++r) ps += p0[r]; for (int r = 0; r < 16; ++r) ps += p1[r];
;   { auto rr = __builtin_amdgcn_permlane32_swap(__float_as_uint(ps), __float_as_uint(ps), false, false);
;     ps = __uint_as_float(rr[0]) + __uint_as_float(rr[1]); }
;   l_reg += ps;
;     ...
;   PK4(p0, 0, pa0); PK4(p0, 8, pa1); PK4(p1, 0, pa2); PK4(p1, 8, pa3);
;     ...
; }
; __device__ __forceinline__ void qkt(f32x16& p0, f32x16& p1, const LAS char* Ks, const bf16x8* qr, int r32, int hi, float nm) {
; #pragma unroll
;   for (int r = 0; r < 16; ++r) { p0[r] = nm; p1[r] = nm; }
; #pragma unroll
;   for (int d0 = 0; d0 < DQK / 16; ++d0) { int cb = (d0 * 16 + hi * 8) * 2;
;     bf16x8 b0 = *reinterpret_cast<const LAS bf16x8*>(Ks + KSWZ(r32, cb));
;     bf16x8 b1 = *reinterpret_cast<const LAS bf16x8*>(Ks + KSWZ(32 + r32, cb));
;     __builtin_amdgcn_s_setprio(1);
;     p0 = __builtin_amdgcn_mfma_f32_32x32x16_bf16(b0, qr[d0], p0, 0, 0, 0);
;     p1 = __builtin_amdgcn_mfma_f32_32x32x16_bf16(b1, qr[d0], p1, 0, 0, 0);
;     __builtin_amdgcn_s_setprio(0); }
; }
; __device__ __forceinline__ void attn_body(const bf16_t* __restrict__ Qb, const bf16_t* __restrict__ Kh, const bf16_t* __restrict__ Vh, unsigned char* __restrict__ Ob, int ldo, int seq, LAS char* lds, const int wv, const float kbound, const float oscale) {
;     ...
;   SLOAD(0); SWRITE(0); SLOAD(KVBLK); SWRITE(1); SLOAD(2 * KVBLK); SWRITE(2); __syncthreads();
;   qkt(pA0, pA1, K_lds, qr, r32, hi, nm); partialSM(pA0, pA1);
;   int b0 = 0, b1 = 1, b2 = 2;
; #pragma unroll 1
;   for (int j = 0; j < NT; j += 2) {
;     SBAR(); qkt(pB0, pB1, K_lds + b1 * SHM_K, qr, r32, hi, nm);
;     finishSM(pA0, pA1, l_reg, pa0, pa1, pa2, pa3); SBAR();
;     if (j + 3 < NT) SLOAD((j + 3) * KVBLK); SBAR();
	v_mfma_f32_32x32x16_bf16 v[64:79], v[24:27], v[144:147], v[64:79]
	s_add_i32 s6, s16, s17
	s_nop 7
	v_exp_f32_e32 v80, v0
	v_exp_f32_e32 v81, v1
	v_exp_f32_e32 v82, v2
	v_exp_f32_e32 v83, v3
	v_exp_f32_e32 v84, v4
	v_exp_f32_e32 v85, v5
	v_exp_f32_e32 v86, v6
	v_exp_f32_e32 v87, v7
	v_exp_f32_e32 v88, v8
	v_exp_f32_e32 v89, v9
	v_exp_f32_e32 v90, v10
	v_exp_f32_e32 v91, v11
	v_exp_f32_e32 v92, v12
	v_exp_f32_e32 v93, v13
	v_exp_f32_e32 v94, v14
	v_exp_f32_e32 v95, v15
	s_lshl_b64 s[14:15], s[6:7], 8
	v_lshl_add_u64 v[174:175], v[18:19], 0, s[14:15]
	v_and_b32_e32 v0, 15, v173
	s_lshl_b64 s[14:15], s[6:7], 7
	v_lshl_or_b32 v174, v0, 4, v174
	v_lshl_add_u64 v[176:177], v[16:17], 0, s[14:15]
	v_and_b32_e32 v0, 7, v173
	v_lshl_or_b32 v176, v0, 4, v176
	s_mov_b32 s6, 0
	v_mov_b32_e32 v0, 0
	v_mov_b32_e32 v1, v187
	v_mov_b32_e32 v2, v187
	v_mov_b32_e32 v3, v187
	v_mov_b32_e32 v4, v187
	v_mov_b32_e32 v5, v187
	v_mov_b32_e32 v6, v187
	v_mov_b32_e32 v7, v187
	v_mov_b32_e32 v8, v187
	v_mov_b32_e32 v9, v187
	v_mov_b32_e32 v10, v187
	v_mov_b32_e32 v11, v187
	v_mov_b32_e32 v12, v187
	v_mov_b32_e32 v13, v187
	v_mov_b32_e32 v14, v187
	v_mov_b32_e32 v15, v187
	v_mov_b32_e32 v16, 0
	v_mov_b32_e32 v17, v187
	v_mov_b32_e32 v18, v187
	v_mov_b32_e32 v19, v187
	v_mov_b32_e32 v20, v187
	v_mov_b32_e32 v21, v187
	v_mov_b32_e32 v22, v187
	v_mov_b32_e32 v23, v187
	v_mov_b32_e32 v24, v187
	v_mov_b32_e32 v25, v187
	v_mov_b32_e32 v26, v187
	v_mov_b32_e32 v27, v187
	v_mov_b32_e32 v28, v187
	v_mov_b32_e32 v29, v187
	v_mov_b32_e32 v30, v187
	v_mov_b32_e32 v31, v187
.LBB0_3144:
	s_mov_b32 s74, s4
	s_lshl_b32 s4, s72, 14
	s_add_i32 s75, s4, 0
	v_add_u32_e32 v242, s75, v192
	v_add_u32_e32 v238, v242, v198
	ds_read_b128 v[234:237], v238 offset:24576
	ds_read_b128 v[238:241], v238 offset:32768
	v_add_f32_e32 v33, 0, v80
	v_add_f32_e32 v33, v81, v33
	v_add_f32_e32 v33, v82, v33
	v_add_f32_e32 v33, v83, v33
	v_add_f32_e32 v33, v84, v33
	s_waitcnt lgkmcnt(1)
	v_mfma_f32_32x32x16_bf16 v[112:127], v[234:237], v[128:131], v[48:63]
	v_add_f32_e32 v33, v85, v33
	v_add_f32_e32 v33, v86, v33
	v_add_f32_e32 v33, v87, v33
	v_add_f32_e32 v33, v88, v33
	s_waitcnt lgkmcnt(0)
	v_mfma_f32_32x32x16_bf16 v[96:111], v[238:241], v[128:131], v[48:63]
	v_add_f32_e32 v33, v89, v33
	v_add_f32_e32 v33, v90, v33
	v_add_f32_e32 v33, v91, v33
	v_add_u32_e32 v238, v242, v199
	ds_read_b128 v[234:237], v238 offset:24576
	ds_read_b128 v[238:241], v238 offset:32768
	v_exp_f32_e32 v64, v64
	v_add_f32_e32 v33, v92, v33
	v_exp_f32_e32 v65, v65
	v_add_f32_e32 v33, v93, v33
	v_exp_f32_e32 v66, v66
	s_waitcnt lgkmcnt(1)
	v_mfma_f32_32x32x16_bf16 v[112:127], v[234:237], v[132:135], v[112:127]
	v_add_f32_e32 v33, v94, v33
	v_exp_f32_e32 v67, v67
	v_add_f32_e32 v33, v95, v33
	v_exp_f32_e32 v68, v68
	s_waitcnt lgkmcnt(0)
	v_mfma_f32_32x32x16_bf16 v[96:111], v[238:241], v[132:135], v[96:111]
	v_add_f32_e32 v33, v64, v33
	v_exp_f32_e32 v69, v69
	v_add_f32_e32 v33, v65, v33
	v_add_u32_e32 v238, v242, v200
	ds_read_b128 v[234:237], v238 offset:24576
	ds_read_b128 v[238:241], v238 offset:32768
	v_exp_f32_e32 v70, v70
	v_add_f32_e32 v33, v66, v33
	v_exp_f32_e32 v71, v71
	v_add_f32_e32 v33, v67, v33
	v_exp_f32_e32 v72, v72
	s_waitcnt lgkmcnt(1)
	v_mfma_f32_32x32x16_bf16 v[112:127], v[234:237], v[136:139], v[112:127]
	v_add_f32_e32 v33, v68, v33
	v_exp_f32_e32 v73, v73
	v_add_f32_e32 v33, v69, v33
	v_exp_f32_e32 v74, v74
	s_waitcnt lgkmcnt(0)
	v_mfma_f32_32x32x16_bf16 v[96:111], v[238:241], v[136:139], v[96:111]
	v_add_f32_e32 v33, v70, v33
	v_exp_f32_e32 v75, v75
	v_add_f32_e32 v33, v71, v33
	v_add_u32_e32 v238, v242, v201
	ds_read_b128 v[234:237], v238 offset:24576
	ds_read_b128 v[238:241], v238 offset:32768
	v_exp_f32_e32 v76, v76
	v_add_f32_e32 v33, v72, v33
	v_exp_f32_e32 v77, v77
	v_add_f32_e32 v33, v73, v33
	v_exp_f32_e32 v78, v78
	s_waitcnt lgkmcnt(1)
	v_mfma_f32_32x32x16_bf16 v[112:127], v[234:237], v[140:143], v[112:127]
	v_add_f32_e32 v33, v74, v33
	v_exp_f32_e32 v79, v79
	v_add_f32_e32 v33, v75, v33
	v_add_f32_e32 v33, v76, v33
	s_waitcnt lgkmcnt(0)
	v_mfma_f32_32x32x16_bf16 v[96:111], v[238:241], v[140:143], v[96:111]
	v_add_f32_e32 v33, v77, v33
	v_add_f32_e32 v33, v78, v33
	v_add_f32_e32 v204, v79, v33
	v_add_u32_e32 v238, v242, v202
	ds_read_b128 v[234:237], v238 offset:24576
	ds_read_b128 v[238:241], v238 offset:32768
	v_mov_b32_e32 v205, v204
	v_cvt_pk_bf16_f32 v34, v80, v81
	v_cvt_pk_bf16_f32 v35, v82, v83
	v_cvt_pk_bf16_f32 v36, v84, v85
	v_cvt_pk_bf16_f32 v37, v86, v87
	s_waitcnt lgkmcnt(1)
	v_mfma_f32_32x32x16_bf16 v[112:127], v[234:237], v[148:151], v[112:127]
	v_cvt_pk_bf16_f32 v38, v88, v89
	v_cvt_pk_bf16_f32 v39, v90, v91
	v_cvt_pk_bf16_f32 v40, v92, v93
	v_cvt_pk_bf16_f32 v41, v94, v95
	s_waitcnt lgkmcnt(0)
	v_mfma_f32_32x32x16_bf16 v[96:111], v[238:241], v[148:151], v[96:111]
	v_cvt_pk_bf16_f32 v42, v64, v65
	v_cvt_pk_bf16_f32 v43, v66, v67
	v_cvt_pk_bf16_f32 v44, v68, v69
	v_add_u32_e32 v242, v242, v203
	ds_read_b128 v[234:237], v242 offset:24576
	ds_read_b128 v[238:241], v242 offset:32768
	v_cvt_pk_bf16_f32 v45, v70, v71
	v_cvt_pk_bf16_f32 v164, v72, v73
	v_cvt_pk_bf16_f32 v165, v74, v75
	v_cvt_pk_bf16_f32 v166, v76, v77
	v_cvt_pk_bf16_f32 v167, v78, v79
	s_waitcnt lgkmcnt(1)
	v_mfma_f32_32x32x16_bf16 v[112:127], v[234:237], v[144:147], v[112:127]
	s_nop 1
	v_permlane32_swap_b32_e32 v204, v205
	v_permlane32_swap_b32_e32 v34, v36
	v_permlane32_swap_b32_e32 v35, v37
	s_waitcnt lgkmcnt(0)
	v_mfma_f32_32x32x16_bf16 v[96:111], v[238:241], v[144:147], v[96:111]
	v_permlane32_swap_b32_e32 v38, v40
	v_permlane32_swap_b32_e32 v39, v41
	v_permlane32_swap_b32_e32 v42, v44
	v_permlane32_swap_b32_e32 v43, v45
	v_permlane32_swap_b32_e32 v164, v166
	v_permlane32_swap_b32_e32 v165, v167
	s_cmp_lt_u32 s73, 61
	s_cselect_b64 s[4:5], -1, 0
	s_cmp_gt_u32 s73, 60
	v_lshl_add_u64 v[180:181], s[22:23], 0, v[176:177]
	v_lshl_add_u64 v[178:179], s[22:23], 0, v[174:175]
	s_cbranch_scc1 .LBB0_3146
	v_add_co_u32_e32 v46, vcc, 0x66006000, v180
	s_nop 1
	v_addc_co_u32_e32 v47, vcc, 0, v181, vcc
	s_waitcnt vmcnt(1)
	v_add_co_u32_e32 v156, vcc, 0x6200c000, v178
	s_nop 1
	v_addc_co_u32_e32 v157, vcc, 0, v179, vcc
	global_load_dwordx4 v[152:155], v[46:47], off
	s_nop 0
	global_load_dwordx4 v[156:159], v[156:157], off
	v_add_co_u32_e32 v46, vcc, 0x6200e000, v178
	s_nop 1
	v_addc_co_u32_e32 v47, vcc, 0, v179, vcc
	global_load_dwordx4 v[160:163], v[46:47], off

; #define LAS __attribute__((address_space(3)))
; #define SBAR() __builtin_amdgcn_sched_barrier(0)
; __device__ __forceinline__ void finishSM(f32x16& p0, f32x16& p1, float& l_reg, bf16x8& pa0, bf16x8& pa1, bf16x8& pa2, bf16x8& pa3) {
;   for (int r = 0; r < 16; ++r) p1[r] = __builtin_amdgcn_exp2f(p1[r]);
;   float ps = 0; for (int r = 0; r < 16; ++r) ps += p0[r]; for (int r = 0; r < 16; ++r) ps += p1[r];
;   { auto rr = __builtin_amdgcn_permlane32_swap(__float_as_uint(ps), __float_as_uint(ps), false, false);
;     ps = __uint_as_float(rr[0]) + __uint_as_float(rr[1]); }
;   l_reg += ps;
;     ...
;   PK4(p0, 0, pa0); PK4(p0, 8, pa1); PK4(p1, 0, pa2); PK4(p1, 8, pa3);
;     ...
; }
; __device__ __forceinline__ void qkt(f32x16& p0, f32x16& p1, const LAS char* Ks, const bf16x8* qr, int r32, int hi, float nm) {
; #pragma unroll
;   for (int r = 0; r < 16; ++r) { p0[r] = nm; p1[r] = nm; }
; #pragma unroll
;   for (int d0 = 0; d0 < DQK / 16; ++d0) { int cb = (d0 * 16 + hi * 8) * 2;
;     bf16x8 b0 = *reinterpret_cast<const LAS bf16x8*>(Ks + KSWZ(r32, cb));
;     bf16x8 b1 = *reinterpret_cast<const LAS bf16x8*>(Ks + KSWZ(32 + r32, cb));
;     __builtin_amdgcn_s_setprio(1);
;     p0 = __builtin_amdgcn_mfma_f32_32x32x16_bf16(b0, qr[d0], p0, 0, 0, 0);
;     p1 = __builtin_amdgcn_mfma_f32_32x32x16_bf16(b1, qr[d0], p1, 0, 0, 0);
;     __builtin_amdgcn_s_setprio(0); }
; }
; __device__ __forceinline__ void attn_body(const bf16_t* __restrict__ Qb, const bf16_t* __restrict__ Kh, const bf16_t* __restrict__ Vh, unsigned char* __restrict__ Ob, int ldo, int seq, LAS char* lds, const int wv, const float kbound, const float oscale) {
;     ...
;     SBAR(); if (j + 2 < NT) qkt(pA0, pA1, K_lds + b2 * SHM_K, qr, r32, hi, nm);
;     finishSM(pB0, pB1, l_reg, pa0, pa1, pa2, pa3); SBAR();
.LBB0_3148:
	s_cmp_lt_u32 s73, 62
	s_cselect_b64 s[14:15], -1, 0
	s_cmp_gt_u32 s73, 61
	s_cselect_b64 s[4:5], -1, 0
	s_and_b64 vcc, exec, s[4:5]
	s_cbranch_vccnz .Lattn1_s2only
	v_lshl_add_u32 v243, s74, 14, v193
	v_add_u32_e32 v238, v243, v198
	ds_read_b128 v[234:237], v238 offset:24576
	ds_read_b128 v[238:241], v238 offset:32768
	v_exp_f32_e32 v34, v112
	v_exp_f32_e32 v35, v113
	v_exp_f32_e32 v36, v114
	v_exp_f32_e32 v37, v115
	v_exp_f32_e32 v38, v116
	v_add_f32_e32 v33, 0, v34
	v_exp_f32_e32 v39, v117
	s_waitcnt lgkmcnt(1)
	v_mfma_f32_32x32x16_bf16 v[80:95], v[234:237], v[128:131], v[48:63]
	v_add_f32_e32 v33, v35, v33
	v_exp_f32_e32 v40, v118
	v_add_f32_e32 v33, v36, v33
	v_exp_f32_e32 v41, v119
	v_add_f32_e32 v33, v37, v33
	s_waitcnt lgkmcnt(0)
	v_mfma_f32_32x32x16_bf16 v[64:79], v[238:241], v[128:131], v[48:63]
	v_exp_f32_e32 v42, v120
	v_add_f32_e32 v33, v38, v33
	v_exp_f32_e32 v43, v121
	v_add_f32_e32 v33, v39, v33
	v_add_u32_e32 v238, v243, v199
	ds_read_b128 v[234:237], v238 offset:24576
	ds_read_b128 v[238:241], v238 offset:32768
	v_exp_f32_e32 v44, v122
	v_add_f32_e32 v33, v40, v33
	v_exp_f32_e32 v45, v123
	v_add_f32_e32 v33, v41, v33
	v_exp_f32_e32 v47, v124
	v_add_f32_e32 v33, v42, v33
	v_exp_f32_e32 v112, v125
	s_waitcnt lgkmcnt(1)
	v_mfma_f32_32x32x16_bf16 v[80:95], v[234:237], v[132:135], v[80:95]
	v_add_f32_e32 v33, v43, v33
	v_exp_f32_e32 v113, v126
	v_add_f32_e32 v33, v44, v33
	v_exp_f32_e32 v114, v127
	v_add_f32_e32 v33, v45, v33
	s_waitcnt lgkmcnt(0)
	v_mfma_f32_32x32x16_bf16 v[64:79], v[238:241], v[132:135], v[64:79]
	v_exp_f32_e32 v96, v96
	v_add_f32_e32 v33, v47, v33
	v_exp_f32_e32 v97, v97
	v_add_f32_e32 v33, v112, v33
	v_add_u32_e32 v238, v243, v200
	ds_read_b128 v[234:237], v238 offset:24576
	ds_read_b128 v[238:241], v238 offset:32768
	v_exp_f32_e32 v98, v98
	v_add_f32_e32 v33, v113, v33
	v_exp_f32_e32 v99, v99
	v_add_f32_e32 v33, v114, v33
	v_exp_f32_e32 v100, v100
	v_add_f32_e32 v33, v96, v33
	v_exp_f32_e32 v101, v101
	s_waitcnt lgkmcnt(1)
	v_mfma_f32_32x32x16_bf16 v[80:95], v[234:237], v[136:139], v[80:95]
	v_add_f32_e32 v33, v97, v33
	v_exp_f32_e32 v102, v102
	v_add_f32_e32 v33, v98, v33
	v_exp_f32_e32 v103, v103
	v_add_f32_e32 v33, v99, v33
	s_waitcnt lgkmcnt(0)
	v_mfma_f32_32x32x16_bf16 v[64:79], v[238:241], v[136:139], v[64:79]
	v_exp_f32_e32 v104, v104
	v_add_f32_e32 v33, v100, v33
	v_exp_f32_e32 v105, v105
	v_add_f32_e32 v33, v101, v33
	v_add_u32_e32 v238, v243, v201
	ds_read_b128 v[234:237], v238 offset:24576
	ds_read_b128 v[238:241], v238 offset:32768
	v_exp_f32_e32 v106, v106
	v_add_f32_e32 v33, v102, v33
	v_exp_f32_e32 v107, v107
	v_add_f32_e32 v33, v103, v33
	v_exp_f32_e32 v108, v108
	v_add_f32_e32 v33, v104, v33
	v_exp_f32_e32 v109, v109
	s_waitcnt lgkmcnt(1)
	v_mfma_f32_32x32x16_bf16 v[80:95], v[234:237], v[140:143], v[80:95]
	v_add_f32_e32 v33, v105, v33
	v_exp_f32_e32 v110, v110
	v_add_f32_e32 v33, v106, v33
	v_exp_f32_e32 v111, v111
	v_add_f32_e32 v33, v107, v33
	s_waitcnt lgkmcnt(0)
	v_mfma_f32_32x32x16_bf16 v[64:79], v[238:241], v[140:143], v[64:79]
	v_add_f32_e32 v33, v108, v33
	v_add_f32_e32 v33, v109, v33
	v_add_f32_e32 v33, v110, v33
	v_add_f32_e32 v33, v111, v33
	v_add_u32_e32 v238, v243, v202
	ds_read_b128 v[234:237], v238 offset:24576
	ds_read_b128 v[238:241], v238 offset:32768
	v_mov_b32_e32 v46, v33
	v_cvt_pk_bf16_f32 v34, v34, v35
	v_cvt_pk_bf16_f32 v35, v36, v37
	v_cvt_pk_bf16_f32 v36, v38, v39
	v_cvt_pk_bf16_f32 v37, v40, v41
	v_cvt_pk_bf16_f32 v38, v42, v43
	v_cvt_pk_bf16_f32 v39, v44, v45
	s_waitcnt lgkmcnt(1)
	v_mfma_f32_32x32x16_bf16 v[80:95], v[234:237], v[148:151], v[80:95]
	v_cvt_pk_bf16_f32 v40, v47, v112
	v_cvt_pk_bf16_f32 v41, v113, v114
	v_cvt_pk_bf16_f32 v42, v96, v97
	v_cvt_pk_bf16_f32 v43, v98, v99
	v_cvt_pk_bf16_f32 v44, v100, v101
	s_waitcnt lgkmcnt(0)
	v_mfma_f32_32x32x16_bf16 v[64:79], v[238:241], v[148:151], v[64:79]
	v_cvt_pk_bf16_f32 v45, v102, v103
	v_cvt_pk_bf16_f32 v96, v104, v105
	v_cvt_pk_bf16_f32 v97, v106, v107
	v_cvt_pk_bf16_f32 v98, v108, v109
	v_add_u32_e32 v238, v243, v203
	ds_read_b128 v[234:237], v238 offset:24576
	ds_read_b128 v[238:241], v238 offset:32768
	v_cvt_pk_bf16_f32 v99, v110, v111
	s_nop 1
	v_permlane32_swap_b32_e32 v33, v46
	v_permlane32_swap_b32_e32 v34, v36
	v_permlane32_swap_b32_e32 v35, v37
	v_permlane32_swap_b32_e32 v38, v40
	v_permlane32_swap_b32_e32 v39, v41
	s_waitcnt lgkmcnt(1)
	v_mfma_f32_32x32x16_bf16 v[80:95], v[234:237], v[144:147], v[80:95]
	v_permlane32_swap_b32_e32 v42, v44
	v_permlane32_swap_b32_e32 v43, v45
	v_permlane32_swap_b32_e32 v96, v98
	v_permlane32_swap_b32_e32 v97, v99
	s_waitcnt lgkmcnt(0)
	v_mfma_f32_32x32x16_bf16 v[64:79], v[238:241], v[144:147], v[64:79]
	s_branch .Lattn1_join

; #define SBAR() __builtin_amdgcn_sched_barrier(0)
; template <int D0> __device__ __forceinline__ void pv_one(f32x16& od, int vb, bf16x8 pa0, bf16x8 pa1, bf16x8 pa2, bf16x8 pa3) {
;   const s16x4 l0 = tr_read<v_rd_off(D0, 0, 0)>(vb), h0 = tr_read<v_rd_off(D0, 0, 1)>(vb), l1 = tr_read<v_rd_off(D0, 1, 0)>(vb), h1 = tr_read<v_rd_off(D0, 1, 1)>(vb);
;   const s16x4 l2 = tr_read<v_rd_off(D0, 2, 0)>(vb), h2 = tr_read<v_rd_off(D0, 2, 1)>(vb), l3 = tr_read<v_rd_off(D0, 3, 0)>(vb), h3 = tr_read<v_rd_off(D0, 3, 1)>(vb);
;   asm volatile("s_waitcnt lgkmcnt(0)" ::: "memory"); SBAR();
;     ...
;   __builtin_amdgcn_s_setprio(1);
;   od = __builtin_amdgcn_mfma_f32_32x32x16_bf16(pa0, PK(l0, h0), od, 0, 0, 0);
;   od = __builtin_amdgcn_mfma_f32_32x32x16_bf16(pa1, PK(l1, h1), od, 0, 0, 0);
;   od = __builtin_amdgcn_mfma_f32_32x32x16_bf16(pa2, PK(l2, h2), od, 0, 0, 0);
;   od = __builtin_amdgcn_mfma_f32_32x32x16_bf16(pa3, PK(l3, h3), od, 0, 0, 0);
;   __builtin_amdgcn_s_setprio(0);
;     ...
; }
; __device__ __forceinline__ void attn_body(const bf16_t* __restrict__ Qb, const bf16_t* __restrict__ Kh, const bf16_t* __restrict__ Vh, unsigned char* __restrict__ Ob, int ldo, int seq, LAS char* lds, const int wv, const float kbound, const float oscale) {
;     ...
;     pv_d0(o, vb0 + b1 * (int)SHM_V, pa0, pa1, pa2, pa3); if (j + 2 < NT) partialSM(pA0, pA1);
;     __syncthreads();
.LBB0_3152:
	s_lshl_b32 s76, s72, 13
	v_add_u32_e32 v47, s76, v188
	ds_read_b64_tr_b16 v[100:101], v47 offset:0
	ds_read_b64_tr_b16 v[102:103], v47 offset:0x400
	ds_read_b64_tr_b16 v[104:105], v47 offset:0x800
	ds_read_b64_tr_b16 v[106:107], v47 offset:0xc00
	ds_read_b64_tr_b16 v[108:109], v47 offset:0x1000
	ds_read_b64_tr_b16 v[110:111], v47 offset:0x1400
	ds_read_b64_tr_b16 v[112:113], v47 offset:0x1800
	ds_read_b64_tr_b16 v[114:115], v47 offset:0x1c00
	s_waitcnt lgkmcnt(0)
	v_mfma_f32_32x32x16_bf16 v[0:15], v[34:37], v[100:103], v[0:15]
	v_exp_f32_e32 v80, v80
	v_exp_f32_e32 v81, v81
	v_mfma_f32_32x32x16_bf16 v[0:15], v[38:41], v[104:107], v[0:15]
	v_exp_f32_e32 v82, v82
	v_exp_f32_e32 v83, v83
	v_mfma_f32_32x32x16_bf16 v[0:15], v[42:45], v[108:111], v[0:15]
	v_exp_f32_e32 v84, v84
	v_exp_f32_e32 v85, v85
	v_mfma_f32_32x32x16_bf16 v[0:15], v[96:99], v[112:115], v[0:15]
	v_exp_f32_e32 v86, v86
	v_exp_f32_e32 v87, v87
	ds_read_b64_tr_b16 v[100:101], v47 offset:0x200
	ds_read_b64_tr_b16 v[102:103], v47 offset:0x600
	ds_read_b64_tr_b16 v[104:105], v47 offset:0xa00
	ds_read_b64_tr_b16 v[106:107], v47 offset:0xe00
	ds_read_b64_tr_b16 v[108:109], v47 offset:0x1200
	ds_read_b64_tr_b16 v[110:111], v47 offset:0x1600
	ds_read_b64_tr_b16 v[112:113], v47 offset:0x1a00
	ds_read_b64_tr_b16 v[114:115], v47 offset:0x1e00
	s_waitcnt lgkmcnt(0)
	v_mfma_f32_32x32x16_bf16 v[16:31], v[34:37], v[100:103], v[16:31]
	v_exp_f32_e32 v88, v88
	v_exp_f32_e32 v89, v89
	v_mfma_f32_32x32x16_bf16 v[16:31], v[38:41], v[104:107], v[16:31]
	v_exp_f32_e32 v90, v90
	v_exp_f32_e32 v91, v91
	v_mfma_f32_32x32x16_bf16 v[16:31], v[42:45], v[108:111], v[16:31]
	v_exp_f32_e32 v92, v92
	v_exp_f32_e32 v93, v93
	v_mfma_f32_32x32x16_bf16 v[16:31], v[96:99], v[112:115], v[16:31]
	v_exp_f32_e32 v94, v94
	v_exp_f32_e32 v95, v95
